# attention tasks: static s_setprio 2 for waves 4-7 (the SIMD partners of waves 0-3) for the whole task, reset at task end, so the barrier-aligned MFMA and softmax VALU blocks of the two waves per SIMD
# baseline (speedup 1.0000x reference)
; __device__ __forceinline__ unsigned pk2(float lo, float hi) { return f2bf(lo) | (f2bf(hi) << 16); }
; __device__ __forceinline__ float rq_sum(float v) { v += __shfl_xor(v, 16); v += __shfl_xor(v, 32); return v; }
; __device__ __forceinline__ float frsq(float x) { return __builtin_amdgcn_rsqf(x); }
; __device__ __forceinline__ void attn_wg_task(const Frame& F, int l, int task) {
;     ...
; #pragma unroll
;     for (int qb = 0; qb < 2; ++qb) {
;         const int tq = tq0 + qb * 16;
;         const float inv = 1.0f / rq_sum(l_run[qb]);
;         float ss = 0.f;
; #pragma unroll
;         for (int db = 0; db < 8; ++db) { O[qb][db] *= inv; ss += (O[qb][db][0] * O[qb][db][0] + O[qb][db][1] * O[qb][db][1]) + (O[qb][db][2] * O[qb][db][2] + O[qb][db][3] * O[qb][db][3]); }
;         const float rstd = frsq(rq_sum(ss) * (1.f / HD) + EPS);
; #pragma unroll
;         for (int db = 0; db < 8; ++db) {
;             const int d0 = h * HD + db * 16 + rq * 4;
;             const f32x4 g4 = ld_f4(F.attn_g + l * 1024 + d0);
;             u32x2 o; o.x = pk2(O[qb][db][0] * rstd * g4[0], O[qb][db][1] * rstd * g4[1]); o.y = pk2(O[qb][db][2] * rstd * g4[2], O[qb][db][3] * rstd * g4[3]);
;             st_u2(MIX + (size_t)tq * D + d0, o);
.LBB0_517:
	ds_bpermute_b32 v64, v202, v151
	v_lshl_or_b32 v82, v204, 2, s17
	v_readlane_b32 s2, v251, 53
	v_readlane_b32 s3, v251, 54
	s_waitcnt lgkmcnt(0)
	v_add_f32_e32 v64, v151, v64
	ds_bpermute_b32 v65, v203, v64
	s_barrier
	s_waitcnt lgkmcnt(0)
	v_lshlrev_b32_e32 v184, 1, v82
	v_readlane_b32 s4, v253, 59
	v_add_f32_e32 v64, v64, v65
	v_div_scale_f32 v65, s[0:1], v64, v64, 1.0
	v_rcp_f32_e32 v66, v65
	v_readlane_b32 s5, v253, 60
	v_fma_f32 v67, -v65, v66, 1.0
	v_fmac_f32_e32 v66, v67, v66
	v_div_scale_f32 v67, vcc, 1.0, v64, 1.0
	v_mul_f32_e32 v68, v67, v66
	v_fma_f32 v69, -v65, v68, v67
	v_fmac_f32_e32 v68, v69, v66
	v_fma_f32 v65, -v65, v68, v67
	v_div_fmas_f32 v65, v65, v66, v68
	v_div_fixup_f32 v84, v65, v64, 1.0
	v_pk_mul_f32 v[80:81], v[32:33], v[84:85] op_sel_hi:[1,0]
	v_pk_mul_f32 v[76:77], v[36:37], v[84:85] op_sel_hi:[1,0]
	v_pk_mul_f32 v[78:79], v[34:35], v[84:85] op_sel_hi:[1,0]
	v_pk_mul_f32 v[74:75], v[38:39], v[84:85] op_sel_hi:[1,0]
	v_mov_b32_e32 v34, v81
	v_mov_b32_e32 v35, v77
	v_mov_b32_e32 v32, v80
	v_mov_b32_e32 v33, v76
	v_pk_mul_f32 v[34:35], v[34:35], v[34:35]
	v_mov_b32_e32 v36, v79
	v_mov_b32_e32 v37, v75
	v_pk_fma_f32 v[32:33], v[32:33], v[32:33], v[34:35]
	v_mov_b32_e32 v34, v78
	v_mov_b32_e32 v35, v74
	v_pk_mul_f32 v[36:37], v[36:37], v[36:37]
	v_pk_mul_f32 v[72:73], v[40:41], v[84:85] op_sel_hi:[1,0]
	v_pk_fma_f32 v[34:35], v[34:35], v[34:35], v[36:37]
	v_pk_mul_f32 v[70:71], v[42:43], v[84:85] op_sel_hi:[1,0]
	v_pk_add_f32 v[32:33], v[32:33], v[34:35]
	v_pk_mul_f32 v[34:35], v[70:71], v[70:71]
	v_pk_add_f32 v[32:33], v[32:33], v[32:33] op_sel_hi:[0,1]
	v_pk_mul_f32 v[36:37], v[72:73], v[72:73]
	v_pk_mul_f32 v[68:69], v[44:45], v[84:85] op_sel_hi:[1,0]
	v_pk_mov_b32 v[38:39], v[36:37], v[34:35] op_sel:[1,0]
	v_mov_b32_e32 v37, v35
	v_pk_mul_f32 v[66:67], v[46:47], v[84:85] op_sel_hi:[1,0]
	v_mul_f32_e32 v32, v68, v68
	v_pk_add_f32 v[34:35], v[38:39], v[36:37]
	v_pk_fma_f32 v[36:37], v[68:69], v[68:69], v[32:33] op_sel_hi:[1,1,0]
	v_mul_f32_e32 v32, v66, v66
	v_pk_add_f32 v[34:35], v[34:35], v[34:35] op_sel_hi:[0,1]
	v_pk_fma_f32 v[38:39], v[66:67], v[66:67], v[32:33] op_sel_hi:[1,1,0]
	v_pk_mul_f32 v[50:51], v[50:51], v[84:85] op_sel_hi:[1,0]
	v_pk_mul_f32 v[64:65], v[48:49], v[84:85] op_sel_hi:[1,0]
	v_mul_f32_e32 v34, v50, v50
	v_mul_f32_e32 v36, v64, v64
	v_mul_f32_e32 v38, v65, v65
	v_mul_f32_e32 v32, v51, v51
	v_pk_add_f32 v[36:37], v[36:37], v[38:39]
	v_pk_add_f32 v[32:33], v[34:35], v[32:33]
	v_pk_mul_f32 v[48:49], v[52:53], v[84:85] op_sel_hi:[1,0]
	v_pk_add_f32 v[32:33], v[36:37], v[32:33]
	v_pk_mul_f32 v[46:47], v[54:55], v[84:85] op_sel_hi:[1,0]
	v_pk_add_f32 v[32:33], v[32:33], v[32:33] op_sel_hi:[0,1]
	v_pk_mul_f32 v[34:35], v[46:47], v[46:47]
	v_pk_mul_f32 v[36:37], v[48:49], v[48:49]
	v_pk_mul_f32 v[44:45], v[56:57], v[84:85] op_sel_hi:[1,0]
	v_pk_mov_b32 v[38:39], v[36:37], v[34:35] op_sel:[1,0]
	v_mov_b32_e32 v37, v35
	v_pk_mul_f32 v[42:43], v[58:59], v[84:85] op_sel_hi:[1,0]
	v_mul_f32_e32 v32, v44, v44
	v_pk_add_f32 v[34:35], v[38:39], v[36:37]
	v_pk_fma_f32 v[40:41], v[44:45], v[44:45], v[32:33] op_sel_hi:[1,1,0]
	v_mul_f32_e32 v32, v42, v42
	v_pk_add_f32 v[34:35], v[34:35], v[34:35] op_sel_hi:[0,1]
	v_pk_fma_f32 v[52:53], v[42:43], v[42:43], v[32:33] op_sel_hi:[1,1,0]
	v_pk_mul_f32 v[36:37], v[62:63], v[84:85] op_sel_hi:[1,0]
	v_pk_mul_f32 v[38:39], v[60:61], v[84:85] op_sel_hi:[1,0]
	v_mul_f32_e32 v34, v36, v36
	v_mul_f32_e32 v40, v38, v38
	v_mul_f32_e32 v52, v39, v39
	v_mul_f32_e32 v32, v37, v37
	v_pk_add_f32 v[40:41], v[40:41], v[52:53]
	v_pk_add_f32 v[32:33], v[34:35], v[32:33]
	v_lshlrev_b32_e32 v54, 2, v82
	global_load_dwordx4 v[96:99], v54, s[42:43]
	global_load_dwordx4 v[100:103], v54, s[42:43] offset:64
	global_load_dwordx4 v[104:107], v54, s[42:43] offset:128
	global_load_dwordx4 v[108:111], v54, s[42:43] offset:192
	global_load_dwordx4 v[112:115], v54, s[42:43] offset:256
	global_load_dwordx4 v[116:119], v54, s[42:43] offset:320
	global_load_dwordx4 v[120:123], v54, s[42:43] offset:384
	global_load_dwordx4 v[124:127], v54, s[42:43] offset:448
	v_pk_add_f32 v[32:33], v[40:41], v[32:33]
	v_mov_b32_e32 v56, v80
	v_add_f32_e32 v32, v32, v33
	ds_bpermute_b32 v33, v202, v32
	v_mov_b32_e32 v57, v78
	v_mov_b32_e32 v78, v81
	s_waitcnt lgkmcnt(0)
	v_add_f32_e32 v32, v32, v33
	ds_bpermute_b32 v33, v203, v32
	s_waitcnt lgkmcnt(0)
	v_add_f32_e32 v32, v32, v33
	v_fmamk_f32 v32, v32, 0x3c000000, v214
	v_rsq_f32_e32 v40, v32
	v_lshlrev_b64 v[32:33], 12, v[152:153]
	v_lshl_add_u64 v[52:53], s[2:3], 0, v[32:33]
	s_waitcnt vmcnt(0)
; __device__ __forceinline__ unsigned pk2(float lo, float hi) { return f2bf(lo) | (f2bf(hi) << 16); }
; __device__ __forceinline__ float rq_sum(float v) { v += __shfl_xor(v, 16); v += __shfl_xor(v, 32); return v; }
; __device__ __forceinline__ float frsq(float x) { return __builtin_amdgcn_rsqf(x); }
; __device__ __forceinline__ void attn_wg_task(const Frame& F, int l, int task) {
;     ...
;         const float rstd = frsq(rq_sum(ss) * (1.f / HD) + EPS);
; #pragma unroll
;         for (int db = 0; db < 8; ++db) {
;             const int d0 = h * HD + db * 16 + rq * 4;
;             const f32x4 g4 = ld_f4(F.attn_g + l * 1024 + d0);
;             u32x2 o; o.x = pk2(O[qb][db][0] * rstd * g4[0], O[qb][db][1] * rstd * g4[1]); o.y = pk2(O[qb][db][2] * rstd * g4[2], O[qb][db][3] * rstd * g4[3]);
;             st_u2(MIX + (size_t)tq * D + d0, o);
	v_mov_b32_e32 v32, v96
	v_mov_b32_e32 v33, v97
	v_mov_b32_e32 v34, v98
	v_mov_b32_e32 v35, v99
	v_pk_mul_f32 v[56:57], v[56:57], v[40:41] op_sel_hi:[1,0]
	v_mov_b32_e32 v58, v32
	v_mov_b32_e32 v59, v34
	v_pk_mul_f32 v[56:57], v[58:59], v[56:57]
	v_pk_mul_f32 v[58:59], v[78:79], v[40:41] op_sel_hi:[1,0]
	v_mov_b32_e32 v34, v33
	v_pk_mul_f32 v[32:33], v[34:35], v[58:59]
	v_and_b32_sdwa v35, v56, v213 dst_sel:DWORD dst_unused:UNUSED_PAD src0_sel:WORD_1 src1_sel:DWORD
	v_add3_u32 v41, v56, v35, s76
	v_and_b32_sdwa v35, v33, v213 dst_sel:DWORD dst_unused:UNUSED_PAD src0_sel:WORD_1 src1_sel:DWORD
	v_and_b32_sdwa v55, v32, v213 dst_sel:DWORD dst_unused:UNUSED_PAD src0_sel:WORD_1 src1_sel:DWORD
	v_and_b32_sdwa v34, v57, v213 dst_sel:DWORD dst_unused:UNUSED_PAD src0_sel:WORD_1 src1_sel:DWORD
	v_add3_u32 v33, v33, v35, s76
	v_add3_u32 v32, v32, v55, s76
	v_add3_u32 v34, v57, v34, s76
	v_and_b32_e32 v33, 0xffff0000, v33
	v_and_b32_e32 v32, 0xffff0000, v32
	v_or_b32_sdwa v35, v33, v34 dst_sel:DWORD dst_unused:UNUSED_PAD src0_sel:DWORD src1_sel:WORD_1
	v_or_b32_sdwa v34, v32, v41 dst_sel:DWORD dst_unused:UNUSED_PAD src0_sel:DWORD src1_sel:WORD_1
	v_lshl_add_u64 v[32:33], v[52:53], 0, v[184:185]
	v_and_b32_e32 v128, 15, v211
	v_lshrrev_b32_e32 v129, 4, v211
	v_lshrrev_b32_e32 v134, 6, v212
	v_mul_u32_u24_e32 v134, 0x2200, v134
	v_add_u32_e32 v134, v229, v134
	v_lshlrev_b32_e32 v135, 3, v129
	v_sub_u32_e32 v132, v134, v135
	v_lshlrev_b32_e32 v135, 8, v129
	v_add_u32_e32 v133, v134, v135
	v_lshlrev_b32_e32 v135, 8, v128
	v_sub_u32_e32 v133, v133, v135
	v_mul_u32_u24_e32 v135, 0xff8, v129
	v_mul_u32_u24_e32 v136, 0xff0, v128
	v_sub_u32_e32 v136, v135, v136
	v_ashrrev_i32_e32 v137, 31, v136
	v_lshl_add_u64 v[130:131], v[32:33], 0, v[136:137]
	ds_write_b64 v132, v[34:35]
	v_mov_b32_e32 v56, v100
	v_mov_b32_e32 v57, v101
	v_mov_b32_e32 v58, v102
	v_mov_b32_e32 v59, v103
	v_mov_b32_e32 v34, v76
	v_mov_b32_e32 v35, v74
	v_pk_mul_f32 v[34:35], v[34:35], v[40:41] op_sel_hi:[1,0]
	v_mov_b32_e32 v74, v77
	v_mov_b32_e32 v52, v56
	v_mov_b32_e32 v53, v58
	v_pk_mul_f32 v[34:35], v[52:53], v[34:35]
	v_pk_mul_f32 v[52:53], v[74:75], v[40:41] op_sel_hi:[1,0]
	v_mov_b32_e32 v58, v57
	v_pk_mul_f32 v[52:53], v[58:59], v[52:53]
	v_and_b32_sdwa v41, v35, v213 dst_sel:DWORD dst_unused:UNUSED_PAD src0_sel:WORD_1 src1_sel:DWORD
	v_and_b32_sdwa v55, v34, v213 dst_sel:DWORD dst_unused:UNUSED_PAD src0_sel:WORD_1 src1_sel:DWORD
	v_add3_u32 v34, v34, v55, s76
	v_add3_u32 v35, v35, v41, s76
	v_and_b32_sdwa v41, v53, v213 dst_sel:DWORD dst_unused:UNUSED_PAD src0_sel:WORD_1 src1_sel:DWORD
	v_and_b32_sdwa v55, v52, v213 dst_sel:DWORD dst_unused:UNUSED_PAD src0_sel:WORD_1 src1_sel:DWORD
	v_add3_u32 v41, v53, v41, s76
	v_add3_u32 v52, v52, v55, s76
	v_and_b32_e32 v41, 0xffff0000, v41
	v_and_b32_e32 v52, 0xffff0000, v52
	v_or_b32_sdwa v35, v41, v35 dst_sel:DWORD dst_unused:UNUSED_PAD src0_sel:DWORD src1_sel:WORD_1
	v_or_b32_sdwa v34, v52, v34 dst_sel:DWORD dst_unused:UNUSED_PAD src0_sel:DWORD src1_sel:WORD_1
	ds_write_b64 v132, v[34:35] offset:32
	v_mov_b32_e32 v56, v104
	v_mov_b32_e32 v57, v105
	v_mov_b32_e32 v58, v106
	v_mov_b32_e32 v59, v107
	v_mov_b32_e32 v34, v72
	v_mov_b32_e32 v35, v70
	v_pk_mul_f32 v[34:35], v[34:35], v[40:41] op_sel_hi:[1,0]
	v_mov_b32_e32 v70, v73
	v_mov_b32_e32 v52, v56
	v_mov_b32_e32 v53, v58
	v_pk_mul_f32 v[34:35], v[52:53], v[34:35]
	v_pk_mul_f32 v[52:53], v[70:71], v[40:41] op_sel_hi:[1,0]
	v_mov_b32_e32 v58, v57
	v_pk_mul_f32 v[52:53], v[58:59], v[52:53]
	v_and_b32_sdwa v41, v35, v213 dst_sel:DWORD dst_unused:UNUSED_PAD src0_sel:WORD_1 src1_sel:DWORD
	v_and_b32_sdwa v55, v34, v213 dst_sel:DWORD dst_unused:UNUSED_PAD src0_sel:WORD_1 src1_sel:DWORD
	v_add3_u32 v34, v34, v55, s76
	v_add3_u32 v35, v35, v41, s76
	v_and_b32_sdwa v41, v53, v213 dst_sel:DWORD dst_unused:UNUSED_PAD src0_sel:WORD_1 src1_sel:DWORD
	v_and_b32_sdwa v55, v52, v213 dst_sel:DWORD dst_unused:UNUSED_PAD src0_sel:WORD_1 src1_sel:DWORD
	v_add3_u32 v41, v53, v41, s76
	v_add3_u32 v52, v52, v55, s76
	v_and_b32_e32 v41, 0xffff0000, v41
	v_and_b32_e32 v52, 0xffff0000, v52
	v_or_b32_sdwa v35, v41, v35 dst_sel:DWORD dst_unused:UNUSED_PAD src0_sel:DWORD src1_sel:WORD_1
	v_or_b32_sdwa v34, v52, v34 dst_sel:DWORD dst_unused:UNUSED_PAD src0_sel:DWORD src1_sel:WORD_1
	ds_write_b64 v132, v[34:35] offset:64
	v_mov_b32_e32 v56, v108
	v_mov_b32_e32 v57, v109
	v_mov_b32_e32 v58, v110
	v_mov_b32_e32 v59, v111
	v_mov_b32_e32 v34, v68
	v_mov_b32_e32 v35, v66
	v_pk_mul_f32 v[34:35], v[34:35], v[40:41] op_sel_hi:[1,0]
	v_mov_b32_e32 v66, v69
	v_mov_b32_e32 v52, v56
	v_mov_b32_e32 v53, v58
	v_pk_mul_f32 v[34:35], v[52:53], v[34:35]
	v_pk_mul_f32 v[52:53], v[66:67], v[40:41] op_sel_hi:[1,0]
	v_mov_b32_e32 v58, v57
	v_pk_mul_f32 v[52:53], v[58:59], v[52:53]
	v_and_b32_sdwa v41, v35, v213 dst_sel:DWORD dst_unused:UNUSED_PAD src0_sel:WORD_1 src1_sel:DWORD
	v_and_b32_sdwa v55, v34, v213 dst_sel:DWORD dst_unused:UNUSED_PAD src0_sel:WORD_1 src1_sel:DWORD
	v_add3_u32 v34, v34, v55, s76
	v_add3_u32 v35, v35, v41, s76
	v_and_b32_sdwa v41, v53, v213 dst_sel:DWORD dst_unused:UNUSED_PAD src0_sel:WORD_1 src1_sel:DWORD
	v_and_b32_sdwa v55, v52, v213 dst_sel:DWORD dst_unused:UNUSED_PAD src0_sel:WORD_1 src1_sel:DWORD
	v_add3_u32 v41, v53, v41, s76
	v_add3_u32 v52, v52, v55, s76
	v_and_b32_e32 v41, 0xffff0000, v41
	v_and_b32_e32 v52, 0xffff0000, v52
	v_or_b32_sdwa v35, v41, v35 dst_sel:DWORD dst_unused:UNUSED_PAD src0_sel:DWORD src1_sel:WORD_1
	v_or_b32_sdwa v34, v52, v34 dst_sel:DWORD dst_unused:UNUSED_PAD src0_sel:DWORD src1_sel:WORD_1
	ds_write_b64 v132, v[34:35] offset:96
	v_mov_b32_e32 v56, v112
	v_mov_b32_e32 v57, v113
; __device__ __forceinline__ unsigned pk2(float lo, float hi) { return f2bf(lo) | (f2bf(hi) << 16); }
; __device__ __forceinline__ float rq_sum(float v) { v += __shfl_xor(v, 16); v += __shfl_xor(v, 32); return v; }
; __device__ __forceinline__ void attn_wg_task(const Frame& F, int l, int task) {
;     ...
;         const float inv = 1.0f / rq_sum(l_run[qb]);
;     ...
;         for (int db = 0; db < 8; ++db) {
;             const int d0 = h * HD + db * 16 + rq * 4;
;             const f32x4 g4 = ld_f4(F.attn_g + l * 1024 + d0);
;             u32x2 o; o.x = pk2(O[qb][db][0] * rstd * g4[0], O[qb][db][1] * rstd * g4[1]); o.y = pk2(O[qb][db][2] * rstd * g4[2], O[qb][db][3] * rstd * g4[3]);
;             st_u2(MIX + (size_t)tq * D + d0, o);
;         }
	v_mov_b32_e32 v58, v114
	v_mov_b32_e32 v59, v115
	v_mov_b32_e32 v34, v64
	v_mov_b32_e32 v35, v50
	v_pk_mul_f32 v[34:35], v[34:35], v[40:41] op_sel_hi:[1,0]
	v_mov_b32_e32 v50, v65
	v_pk_mul_f32 v[50:51], v[50:51], v[40:41] op_sel_hi:[1,0]
	v_mov_b32_e32 v52, v56
	v_mov_b32_e32 v53, v58
	v_pk_mul_f32 v[34:35], v[52:53], v[34:35]
	v_mov_b32_e32 v58, v57
	v_pk_mul_f32 v[50:51], v[58:59], v[50:51]
	v_and_b32_sdwa v41, v35, v213 dst_sel:DWORD dst_unused:UNUSED_PAD src0_sel:WORD_1 src1_sel:DWORD
	v_and_b32_sdwa v52, v34, v213 dst_sel:DWORD dst_unused:UNUSED_PAD src0_sel:WORD_1 src1_sel:DWORD
	v_add3_u32 v34, v34, v52, s76
	v_add3_u32 v35, v35, v41, s76
	v_and_b32_sdwa v41, v51, v213 dst_sel:DWORD dst_unused:UNUSED_PAD src0_sel:WORD_1 src1_sel:DWORD
	v_and_b32_sdwa v52, v50, v213 dst_sel:DWORD dst_unused:UNUSED_PAD src0_sel:WORD_1 src1_sel:DWORD
	v_add3_u32 v41, v51, v41, s76
	v_add3_u32 v50, v50, v52, s76
	v_and_b32_e32 v41, 0xffff0000, v41
	v_and_b32_e32 v50, 0xffff0000, v50
	v_or_b32_sdwa v35, v41, v35 dst_sel:DWORD dst_unused:UNUSED_PAD src0_sel:DWORD src1_sel:WORD_1
	v_or_b32_sdwa v34, v50, v34 dst_sel:DWORD dst_unused:UNUSED_PAD src0_sel:DWORD src1_sel:WORD_1
	ds_write_b64 v132, v[34:35] offset:128
	v_mov_b32_e32 v50, v116
	v_mov_b32_e32 v51, v117
	v_mov_b32_e32 v52, v118
	v_mov_b32_e32 v53, v119
	v_mov_b32_e32 v34, v48
	v_mov_b32_e32 v35, v46
	v_pk_mul_f32 v[34:35], v[34:35], v[40:41] op_sel_hi:[1,0]
	v_mov_b32_e32 v46, v49
	v_pk_mul_f32 v[46:47], v[46:47], v[40:41] op_sel_hi:[1,0]
	v_mov_b32_e32 v56, v50
	v_mov_b32_e32 v57, v52
	v_pk_mul_f32 v[34:35], v[56:57], v[34:35]
	v_mov_b32_e32 v52, v51
	v_pk_mul_f32 v[46:47], v[52:53], v[46:47]
	v_and_b32_sdwa v41, v35, v213 dst_sel:DWORD dst_unused:UNUSED_PAD src0_sel:WORD_1 src1_sel:DWORD
	v_and_b32_sdwa v48, v34, v213 dst_sel:DWORD dst_unused:UNUSED_PAD src0_sel:WORD_1 src1_sel:DWORD
	v_add3_u32 v34, v34, v48, s76
	v_add3_u32 v35, v35, v41, s76
	v_and_b32_sdwa v41, v47, v213 dst_sel:DWORD dst_unused:UNUSED_PAD src0_sel:WORD_1 src1_sel:DWORD
	v_and_b32_sdwa v48, v46, v213 dst_sel:DWORD dst_unused:UNUSED_PAD src0_sel:WORD_1 src1_sel:DWORD
	v_add3_u32 v41, v47, v41, s76
	v_add3_u32 v46, v46, v48, s76
	v_and_b32_e32 v41, 0xffff0000, v41
	v_and_b32_e32 v46, 0xffff0000, v46
	v_or_b32_sdwa v35, v41, v35 dst_sel:DWORD dst_unused:UNUSED_PAD src0_sel:DWORD src1_sel:WORD_1
	v_or_b32_sdwa v34, v46, v34 dst_sel:DWORD dst_unused:UNUSED_PAD src0_sel:DWORD src1_sel:WORD_1
	ds_write_b64 v132, v[34:35] offset:160
	v_mov_b32_e32 v46, v120
	v_mov_b32_e32 v47, v121
	v_mov_b32_e32 v48, v122
	v_mov_b32_e32 v49, v123
	v_mov_b32_e32 v34, v44
	v_mov_b32_e32 v35, v42
	v_pk_mul_f32 v[34:35], v[34:35], v[40:41] op_sel_hi:[1,0]
	v_mov_b32_e32 v42, v45
	v_pk_mul_f32 v[42:43], v[42:43], v[40:41] op_sel_hi:[1,0]
	v_mov_b32_e32 v50, v46
	v_mov_b32_e32 v51, v48
	v_pk_mul_f32 v[34:35], v[50:51], v[34:35]
	v_mov_b32_e32 v48, v47
	v_pk_mul_f32 v[42:43], v[48:49], v[42:43]
	v_and_b32_sdwa v41, v35, v213 dst_sel:DWORD dst_unused:UNUSED_PAD src0_sel:WORD_1 src1_sel:DWORD
	v_and_b32_sdwa v44, v34, v213 dst_sel:DWORD dst_unused:UNUSED_PAD src0_sel:WORD_1 src1_sel:DWORD
	v_add3_u32 v34, v34, v44, s76
	v_add3_u32 v35, v35, v41, s76
	v_and_b32_sdwa v41, v43, v213 dst_sel:DWORD dst_unused:UNUSED_PAD src0_sel:WORD_1 src1_sel:DWORD
	v_and_b32_sdwa v44, v42, v213 dst_sel:DWORD dst_unused:UNUSED_PAD src0_sel:WORD_1 src1_sel:DWORD
	v_add3_u32 v41, v43, v41, s76
	v_add3_u32 v42, v42, v44, s76
	v_and_b32_e32 v41, 0xffff0000, v41
	v_and_b32_e32 v42, 0xffff0000, v42
	v_or_b32_sdwa v35, v41, v35 dst_sel:DWORD dst_unused:UNUSED_PAD src0_sel:DWORD src1_sel:WORD_1
	v_or_b32_sdwa v34, v42, v34 dst_sel:DWORD dst_unused:UNUSED_PAD src0_sel:DWORD src1_sel:WORD_1
	ds_write_b64 v132, v[34:35] offset:192
	v_mov_b32_e32 v42, v124
	v_mov_b32_e32 v43, v125
	v_mov_b32_e32 v44, v126
	v_mov_b32_e32 v45, v127
	v_mov_b32_e32 v34, v38
	v_mov_b32_e32 v35, v36
	v_pk_mul_f32 v[34:35], v[34:35], v[40:41] op_sel_hi:[1,0]
	v_mov_b32_e32 v36, v39
	v_pk_mul_f32 v[36:37], v[36:37], v[40:41] op_sel_hi:[1,0]
	v_mov_b32_e32 v46, v42
	v_mov_b32_e32 v47, v44
	v_pk_mul_f32 v[34:35], v[46:47], v[34:35]
	v_mov_b32_e32 v44, v43
	v_pk_mul_f32 v[36:37], v[44:45], v[36:37]
	v_and_b32_sdwa v38, v35, v213 dst_sel:DWORD dst_unused:UNUSED_PAD src0_sel:WORD_1 src1_sel:DWORD
	v_and_b32_sdwa v39, v34, v213 dst_sel:DWORD dst_unused:UNUSED_PAD src0_sel:WORD_1 src1_sel:DWORD
	v_add3_u32 v34, v34, v39, s76
	v_add3_u32 v35, v35, v38, s76
	v_and_b32_sdwa v38, v37, v213 dst_sel:DWORD dst_unused:UNUSED_PAD src0_sel:WORD_1 src1_sel:DWORD
	v_and_b32_sdwa v39, v36, v213 dst_sel:DWORD dst_unused:UNUSED_PAD src0_sel:WORD_1 src1_sel:DWORD
	v_add3_u32 v37, v37, v38, s76
	v_add3_u32 v36, v36, v39, s76
	v_and_b32_e32 v37, 0xffff0000, v37
	v_and_b32_e32 v36, 0xffff0000, v36
	v_or_b32_sdwa v35, v37, v35 dst_sel:DWORD dst_unused:UNUSED_PAD src0_sel:DWORD src1_sel:WORD_1
	v_or_b32_sdwa v34, v36, v34 dst_sel:DWORD dst_unused:UNUSED_PAD src0_sel:DWORD src1_sel:WORD_1
	ds_write_b64 v132, v[34:35] offset:224
	ds_bpermute_b32 v32, v202, v150
	s_waitcnt lgkmcnt(0)
	v_add_f32_e32 v32, v150, v32
	ds_bpermute_b32 v33, v203, v32
	s_waitcnt lgkmcnt(0)
; __device__ __forceinline__ unsigned pk2(float lo, float hi) { return f2bf(lo) | (f2bf(hi) << 16); }
; __device__ __forceinline__ float rq_sum(float v) { v += __shfl_xor(v, 16); v += __shfl_xor(v, 32); return v; }
; __device__ __forceinline__ float frsq(float x) { return __builtin_amdgcn_rsqf(x); }
; __device__ __forceinline__ void attn_wg_task(const Frame& F, int l, int task) {
;     ...
;         const float inv = 1.0f / rq_sum(l_run[qb]);
;         float ss = 0.f;
; #pragma unroll
;         for (int db = 0; db < 8; ++db) { O[qb][db] *= inv; ss += (O[qb][db][0] * O[qb][db][0] + O[qb][db][1] * O[qb][db][1]) + (O[qb][db][2] * O[qb][db][2] + O[qb][db][3] * O[qb][db][3]); }
;         const float rstd = frsq(rq_sum(ss) * (1.f / HD) + EPS);
; #pragma unroll
;         for (int db = 0; db < 8; ++db) {
;             const int d0 = h * HD + db * 16 + rq * 4;
;             const f32x4 g4 = ld_f4(F.attn_g + l * 1024 + d0);
;             u32x2 o; o.x = pk2(O[qb][db][0] * rstd * g4[0], O[qb][db][1] * rstd * g4[1]); o.y = pk2(O[qb][db][2] * rstd * g4[2], O[qb][db][3] * rstd * g4[3]);
;             st_u2(MIX + (size_t)tq * D + d0, o);
;         }
	v_add_f32_e32 v32, v32, v33
	v_div_scale_f32 v33, s[0:1], v32, v32, 1.0
	v_rcp_f32_e32 v34, v33
	s_nop 0
	v_fma_f32 v35, -v33, v34, 1.0
	v_fmac_f32_e32 v34, v35, v34
	v_div_scale_f32 v35, vcc, 1.0, v32, 1.0
	v_mul_f32_e32 v36, v35, v34
	v_fma_f32 v37, -v33, v36, v35
	v_fmac_f32_e32 v36, v37, v34
	v_fma_f32 v33, -v33, v36, v35
	v_div_fmas_f32 v33, v33, v34, v36
	v_div_fixup_f32 v48, v33, v32, 1.0
	v_pk_mul_f32 v[46:47], v[4:5], v[48:49] op_sel_hi:[1,0]
	v_pk_mul_f32 v[42:43], v[8:9], v[48:49] op_sel_hi:[1,0]
	v_pk_mul_f32 v[44:45], v[6:7], v[48:49] op_sel_hi:[1,0]
	v_pk_mul_f32 v[36:37], v[10:11], v[48:49] op_sel_hi:[1,0]
	v_mov_b32_e32 v6, v47
	v_mov_b32_e32 v7, v43
	v_mov_b32_e32 v4, v46
	v_mov_b32_e32 v5, v42
	v_pk_mul_f32 v[6:7], v[6:7], v[6:7]
	v_mov_b32_e32 v8, v45
	v_mov_b32_e32 v9, v37
	v_pk_fma_f32 v[4:5], v[4:5], v[4:5], v[6:7]
	v_mov_b32_e32 v6, v44
	v_mov_b32_e32 v7, v36
	v_pk_mul_f32 v[8:9], v[8:9], v[8:9]
	v_pk_mul_f32 v[40:41], v[0:1], v[48:49] op_sel_hi:[1,0]
	v_pk_mul_f32 v[38:39], v[2:3], v[48:49] op_sel_hi:[1,0]
	v_pk_fma_f32 v[6:7], v[6:7], v[6:7], v[8:9]
	v_pk_mul_f32 v[0:1], v[38:39], v[38:39]
	v_pk_mul_f32 v[2:3], v[40:41], v[40:41]
	v_pk_add_f32 v[4:5], v[4:5], v[6:7]
	v_pk_mov_b32 v[6:7], v[2:3], v[0:1] op_sel:[1,0]
	v_mov_b32_e32 v3, v1
	v_pk_add_f32 v[0:1], v[6:7], v[2:3]
	v_pk_mul_f32 v[34:35], v[12:13], v[48:49] op_sel_hi:[1,0]
	v_pk_add_f32 v[0:1], v[0:1], v[0:1] op_sel_hi:[0,1]
	v_pk_mul_f32 v[32:33], v[14:15], v[48:49] op_sel_hi:[1,0]
	v_mul_f32_e32 v0, v34, v34
	v_pk_fma_f32 v[2:3], v[34:35], v[34:35], v[0:1] op_sel_hi:[1,1,0]
	v_mul_f32_e32 v0, v32, v32
	v_pk_add_f32 v[4:5], v[4:5], v[4:5] op_sel_hi:[0,1]
	v_pk_fma_f32 v[6:7], v[32:33], v[32:33], v[0:1] op_sel_hi:[1,1,0]
	v_pk_mul_f32 v[14:15], v[18:19], v[48:49] op_sel_hi:[1,0]
	v_pk_mul_f32 v[16:17], v[16:17], v[48:49] op_sel_hi:[1,0]
	v_mul_f32_e32 v0, v14, v14
	v_mul_f32_e32 v2, v16, v16
	v_mul_f32_e32 v6, v17, v17
	v_mul_f32_e32 v4, v15, v15
	v_pk_add_f32 v[2:3], v[2:3], v[6:7]
	v_pk_add_f32 v[0:1], v[0:1], v[4:5]
	v_pk_mul_f32 v[12:13], v[20:21], v[48:49] op_sel_hi:[1,0]
	v_pk_add_f32 v[0:1], v[2:3], v[0:1]
	v_pk_mul_f32 v[10:11], v[22:23], v[48:49] op_sel_hi:[1,0]
	v_pk_add_f32 v[4:5], v[0:1], v[0:1] op_sel_hi:[0,1]
	v_pk_mul_f32 v[0:1], v[10:11], v[10:11]
	v_pk_mul_f32 v[2:3], v[12:13], v[12:13]
	v_pk_mul_f32 v[8:9], v[24:25], v[48:49] op_sel_hi:[1,0]
	v_pk_mov_b32 v[6:7], v[2:3], v[0:1] op_sel:[1,0]
	v_mov_b32_e32 v3, v1
	v_pk_add_f32 v[0:1], v[6:7], v[2:3]
	v_pk_mul_f32 v[6:7], v[26:27], v[48:49] op_sel_hi:[1,0]
	v_pk_add_f32 v[18:19], v[0:1], v[0:1] op_sel_hi:[0,1]
	v_mul_f32_e32 v0, v8, v8
	v_pk_fma_f32 v[20:21], v[8:9], v[8:9], v[0:1] op_sel_hi:[1,1,0]
	v_mul_f32_e32 v0, v6, v6
	v_pk_fma_f32 v[22:23], v[6:7], v[6:7], v[0:1] op_sel_hi:[1,1,0]
	v_pk_mul_f32 v[0:1], v[30:31], v[48:49] op_sel_hi:[1,0]
	v_pk_mul_f32 v[2:3], v[28:29], v[48:49] op_sel_hi:[1,0]
	v_mul_f32_e32 v18, v0, v0
	v_mul_f32_e32 v20, v2, v2
	v_mul_f32_e32 v22, v3, v3
	v_mul_f32_e32 v4, v1, v1
	v_pk_add_f32 v[20:21], v[20:21], v[22:23]
	v_pk_add_f32 v[4:5], v[18:19], v[4:5]
	v_mov_b32_e32 v24, v46
	v_pk_add_f32 v[4:5], v[20:21], v[4:5]
	v_mov_b32_e32 v20, v96
	v_mov_b32_e32 v21, v97
	v_mov_b32_e32 v22, v98
	v_mov_b32_e32 v23, v99
	v_add_f32_e32 v4, v4, v5
	ds_bpermute_b32 v5, v202, v4
	v_mov_b32_e32 v25, v44
	v_mov_b32_e32 v44, v47
	v_lshlrev_b64 v[18:19], 12, v[148:149]
	v_lshl_add_u64 v[18:19], s[2:3], 0, v[18:19]
	s_waitcnt lgkmcnt(0)
	v_add_f32_e32 v4, v4, v5
	ds_bpermute_b32 v5, v203, v4
	v_lshl_add_u64 v[18:19], v[18:19], 0, v[184:185]
	s_add_i32 s2, s16, 1
	s_cmp_lt_u32 s16, 2
	s_cselect_b64 s[0:1], -1, 0
	s_waitcnt lgkmcnt(0)
	v_add_f32_e32 v4, v4, v5
	v_fmamk_f32 v4, v4, 0x3c000000, v214
	v_rsq_f32_e32 v4, v4
	s_and_b64 s[0:1], s[4:5], s[0:1]
	s_andn2_b64 vcc, exec, s[0:1]
	s_mov_b32 s16, s2
	v_pk_mul_f32 v[24:25], v[24:25], v[4:5] op_sel_hi:[1,0]
	v_mov_b32_e32 v26, v20
	v_mov_b32_e32 v27, v22
	v_pk_mul_f32 v[24:25], v[26:27], v[24:25]
	v_pk_mul_f32 v[26:27], v[44:45], v[4:5] op_sel_hi:[1,0]
	v_mov_b32_e32 v22, v21
	v_pk_mul_f32 v[20:21], v[22:23], v[26:27]
	v_and_b32_sdwa v22, v24, v213 dst_sel:DWORD dst_unused:UNUSED_PAD src0_sel:WORD_1 src1_sel:DWORD
	v_add3_u32 v22, v24, v22, s76
	v_and_b32_sdwa v23, v21, v213 dst_sel:DWORD dst_unused:UNUSED_PAD src0_sel:WORD_1 src1_sel:DWORD
	v_and_b32_sdwa v24, v20, v213 dst_sel:DWORD dst_unused:UNUSED_PAD src0_sel:WORD_1 src1_sel:DWORD
	v_and_b32_sdwa v5, v25, v213 dst_sel:DWORD dst_unused:UNUSED_PAD src0_sel:WORD_1 src1_sel:DWORD
	v_add3_u32 v21, v21, v23, s76
	v_add3_u32 v20, v20, v24, s76
	v_add3_u32 v5, v25, v5, s76
	v_and_b32_e32 v21, 0xffff0000, v21
	v_and_b32_e32 v20, 0xffff0000, v20
	v_or_b32_sdwa v21, v21, v5 dst_sel:DWORD dst_unused:UNUSED_PAD src0_sel:DWORD src1_sel:WORD_1
	v_or_b32_sdwa v20, v20, v22 dst_sel:DWORD dst_unused:UNUSED_PAD src0_sel:DWORD src1_sel:WORD_1
	ds_write_b64 v132, v[20:21] offset:4352
	v_mov_b32_e32 v20, v100
	v_mov_b32_e32 v21, v101
	v_mov_b32_e32 v22, v102
	v_mov_b32_e32 v23, v103
	v_mov_b32_e32 v24, v42
	v_mov_b32_e32 v25, v36
	v_pk_mul_f32 v[24:25], v[24:25], v[4:5] op_sel_hi:[1,0]
	v_mov_b32_e32 v36, v43
	v_mov_b32_e32 v26, v20
	v_mov_b32_e32 v27, v22
	v_pk_mul_f32 v[24:25], v[26:27], v[24:25]
	v_pk_mul_f32 v[26:27], v[36:37], v[4:5] op_sel_hi:[1,0]
	v_mov_b32_e32 v22, v21
	v_pk_mul_f32 v[20:21], v[22:23], v[26:27]
	v_and_b32_sdwa v22, v24, v213 dst_sel:DWORD dst_unused:UNUSED_PAD src0_sel:WORD_1 src1_sel:DWORD
	v_add3_u32 v22, v24, v22, s76
	v_and_b32_sdwa v23, v21, v213 dst_sel:DWORD dst_unused:UNUSED_PAD src0_sel:WORD_1 src1_sel:DWORD
; __device__ __forceinline__ unsigned pk2(float lo, float hi) { return f2bf(lo) | (f2bf(hi) << 16); }
; __device__ __forceinline__ void attn_wg_task(const Frame& F, int l, int task) {
;     ...
;         for (int db = 0; db < 8; ++db) {
;             const int d0 = h * HD + db * 16 + rq * 4;
;             const f32x4 g4 = ld_f4(F.attn_g + l * 1024 + d0);
;             u32x2 o; o.x = pk2(O[qb][db][0] * rstd * g4[0], O[qb][db][1] * rstd * g4[1]); o.y = pk2(O[qb][db][2] * rstd * g4[2], O[qb][db][3] * rstd * g4[3]);
;             st_u2(MIX + (size_t)tq * D + d0, o);
;         }
	v_and_b32_sdwa v24, v20, v213 dst_sel:DWORD dst_unused:UNUSED_PAD src0_sel:WORD_1 src1_sel:DWORD
	v_and_b32_sdwa v5, v25, v213 dst_sel:DWORD dst_unused:UNUSED_PAD src0_sel:WORD_1 src1_sel:DWORD
	v_add3_u32 v21, v21, v23, s76
	v_add3_u32 v20, v20, v24, s76
	v_add3_u32 v5, v25, v5, s76
	v_and_b32_e32 v21, 0xffff0000, v21
	v_and_b32_e32 v20, 0xffff0000, v20
	v_or_b32_sdwa v21, v21, v5 dst_sel:DWORD dst_unused:UNUSED_PAD src0_sel:DWORD src1_sel:WORD_1
	v_or_b32_sdwa v20, v20, v22 dst_sel:DWORD dst_unused:UNUSED_PAD src0_sel:DWORD src1_sel:WORD_1
	ds_write_b64 v132, v[20:21] offset:4384
	v_mov_b32_e32 v20, v104
	v_mov_b32_e32 v21, v105
	v_mov_b32_e32 v22, v106
	v_mov_b32_e32 v23, v107
	v_mov_b32_e32 v24, v40
	v_mov_b32_e32 v25, v38
	v_pk_mul_f32 v[24:25], v[24:25], v[4:5] op_sel_hi:[1,0]
	v_mov_b32_e32 v38, v41
	v_mov_b32_e32 v26, v20
	v_mov_b32_e32 v27, v22
	v_pk_mul_f32 v[24:25], v[26:27], v[24:25]
	v_pk_mul_f32 v[26:27], v[38:39], v[4:5] op_sel_hi:[1,0]
	v_mov_b32_e32 v22, v21
	v_pk_mul_f32 v[20:21], v[22:23], v[26:27]
	v_and_b32_sdwa v22, v24, v213 dst_sel:DWORD dst_unused:UNUSED_PAD src0_sel:WORD_1 src1_sel:DWORD
	v_add3_u32 v22, v24, v22, s76
	v_and_b32_sdwa v23, v21, v213 dst_sel:DWORD dst_unused:UNUSED_PAD src0_sel:WORD_1 src1_sel:DWORD
	v_and_b32_sdwa v24, v20, v213 dst_sel:DWORD dst_unused:UNUSED_PAD src0_sel:WORD_1 src1_sel:DWORD
	v_and_b32_sdwa v5, v25, v213 dst_sel:DWORD dst_unused:UNUSED_PAD src0_sel:WORD_1 src1_sel:DWORD
	v_add3_u32 v21, v21, v23, s76
	v_add3_u32 v20, v20, v24, s76
	v_add3_u32 v5, v25, v5, s76
	v_and_b32_e32 v21, 0xffff0000, v21
	v_and_b32_e32 v20, 0xffff0000, v20
	v_or_b32_sdwa v21, v21, v5 dst_sel:DWORD dst_unused:UNUSED_PAD src0_sel:DWORD src1_sel:WORD_1
	v_or_b32_sdwa v20, v20, v22 dst_sel:DWORD dst_unused:UNUSED_PAD src0_sel:DWORD src1_sel:WORD_1
	ds_write_b64 v132, v[20:21] offset:4416
	v_mov_b32_e32 v20, v108
	v_mov_b32_e32 v21, v109
	v_mov_b32_e32 v22, v110
	v_mov_b32_e32 v23, v111
	v_mov_b32_e32 v24, v34
	v_mov_b32_e32 v25, v32
	v_pk_mul_f32 v[24:25], v[24:25], v[4:5] op_sel_hi:[1,0]
	v_mov_b32_e32 v32, v35
	v_mov_b32_e32 v26, v20
	v_mov_b32_e32 v27, v22
	v_pk_mul_f32 v[24:25], v[26:27], v[24:25]
	v_pk_mul_f32 v[26:27], v[32:33], v[4:5] op_sel_hi:[1,0]
	v_mov_b32_e32 v22, v21
	v_pk_mul_f32 v[20:21], v[22:23], v[26:27]
	v_and_b32_sdwa v22, v24, v213 dst_sel:DWORD dst_unused:UNUSED_PAD src0_sel:WORD_1 src1_sel:DWORD
	v_add3_u32 v22, v24, v22, s76
	v_and_b32_sdwa v23, v21, v213 dst_sel:DWORD dst_unused:UNUSED_PAD src0_sel:WORD_1 src1_sel:DWORD
	v_and_b32_sdwa v24, v20, v213 dst_sel:DWORD dst_unused:UNUSED_PAD src0_sel:WORD_1 src1_sel:DWORD
	v_and_b32_sdwa v5, v25, v213 dst_sel:DWORD dst_unused:UNUSED_PAD src0_sel:WORD_1 src1_sel:DWORD
	v_add3_u32 v21, v21, v23, s76
	v_add3_u32 v20, v20, v24, s76
	v_add3_u32 v5, v25, v5, s76
	v_and_b32_e32 v21, 0xffff0000, v21
	v_and_b32_e32 v20, 0xffff0000, v20
	v_or_b32_sdwa v21, v21, v5 dst_sel:DWORD dst_unused:UNUSED_PAD src0_sel:DWORD src1_sel:WORD_1
	v_or_b32_sdwa v20, v20, v22 dst_sel:DWORD dst_unused:UNUSED_PAD src0_sel:DWORD src1_sel:WORD_1
	ds_write_b64 v132, v[20:21] offset:4448
	v_mov_b32_e32 v20, v112
	v_mov_b32_e32 v21, v113
	v_mov_b32_e32 v22, v114
	v_mov_b32_e32 v23, v115
	v_mov_b32_e32 v25, v14
	v_mov_b32_e32 v14, v17
	v_mov_b32_e32 v24, v16
	v_pk_mul_f32 v[14:15], v[14:15], v[4:5] op_sel_hi:[1,0]
	v_pk_mul_f32 v[24:25], v[24:25], v[4:5] op_sel_hi:[1,0]
	v_mov_b32_e32 v27, v22
	v_mov_b32_e32 v22, v21
	v_mov_b32_e32 v26, v20
	v_pk_mul_f32 v[14:15], v[22:23], v[14:15]
	v_pk_mul_f32 v[24:25], v[26:27], v[24:25]
	v_and_b32_sdwa v17, v15, v213 dst_sel:DWORD dst_unused:UNUSED_PAD src0_sel:WORD_1 src1_sel:DWORD
	v_and_b32_sdwa v20, v14, v213 dst_sel:DWORD dst_unused:UNUSED_PAD src0_sel:WORD_1 src1_sel:DWORD
	v_and_b32_sdwa v5, v25, v213 dst_sel:DWORD dst_unused:UNUSED_PAD src0_sel:WORD_1 src1_sel:DWORD
	v_and_b32_sdwa v16, v24, v213 dst_sel:DWORD dst_unused:UNUSED_PAD src0_sel:WORD_1 src1_sel:DWORD
	v_add3_u32 v15, v15, v17, s76
	v_add3_u32 v14, v14, v20, s76
	v_add3_u32 v16, v24, v16, s76
	v_add3_u32 v5, v25, v5, s76
	v_and_b32_e32 v15, 0xffff0000, v15
	v_and_b32_e32 v14, 0xffff0000, v14
	v_or_b32_sdwa v15, v15, v5 dst_sel:DWORD dst_unused:UNUSED_PAD src0_sel:DWORD src1_sel:WORD_1
	v_or_b32_sdwa v14, v14, v16 dst_sel:DWORD dst_unused:UNUSED_PAD src0_sel:DWORD src1_sel:WORD_1
	ds_write_b64 v132, v[14:15] offset:4480
	v_mov_b32_e32 v14, v116
	v_mov_b32_e32 v15, v117
	v_mov_b32_e32 v16, v118
	v_mov_b32_e32 v17, v119
	v_mov_b32_e32 v21, v10
	v_mov_b32_e32 v10, v13
	v_mov_b32_e32 v20, v12
	v_pk_mul_f32 v[10:11], v[10:11], v[4:5] op_sel_hi:[1,0]
	v_pk_mul_f32 v[20:21], v[20:21], v[4:5] op_sel_hi:[1,0]
	v_mov_b32_e32 v23, v16
	v_mov_b32_e32 v16, v15
	v_mov_b32_e32 v22, v14
; __device__ __forceinline__ unsigned pk2(float lo, float hi) { return f2bf(lo) | (f2bf(hi) << 16); }
; __device__ __forceinline__ void attn_wg_task(const Frame& F, int l, int task) {
;     ...
;         for (int db = 0; db < 8; ++db) {
;             const int d0 = h * HD + db * 16 + rq * 4;
;             const f32x4 g4 = ld_f4(F.attn_g + l * 1024 + d0);
;             u32x2 o; o.x = pk2(O[qb][db][0] * rstd * g4[0], O[qb][db][1] * rstd * g4[1]); o.y = pk2(O[qb][db][2] * rstd * g4[2], O[qb][db][3] * rstd * g4[3]);
;             st_u2(MIX + (size_t)tq * D + d0, o);
;         }
;     }
	v_pk_mul_f32 v[10:11], v[16:17], v[10:11]
	v_pk_mul_f32 v[20:21], v[22:23], v[20:21]
	v_and_b32_sdwa v13, v11, v213 dst_sel:DWORD dst_unused:UNUSED_PAD src0_sel:WORD_1 src1_sel:DWORD
	v_and_b32_sdwa v14, v10, v213 dst_sel:DWORD dst_unused:UNUSED_PAD src0_sel:WORD_1 src1_sel:DWORD
	v_and_b32_sdwa v5, v21, v213 dst_sel:DWORD dst_unused:UNUSED_PAD src0_sel:WORD_1 src1_sel:DWORD
	v_and_b32_sdwa v12, v20, v213 dst_sel:DWORD dst_unused:UNUSED_PAD src0_sel:WORD_1 src1_sel:DWORD
	v_add3_u32 v11, v11, v13, s76
	v_add3_u32 v10, v10, v14, s76
	v_add3_u32 v12, v20, v12, s76
	v_add3_u32 v5, v21, v5, s76
	v_and_b32_e32 v11, 0xffff0000, v11
	v_and_b32_e32 v10, 0xffff0000, v10
	v_or_b32_sdwa v11, v11, v5 dst_sel:DWORD dst_unused:UNUSED_PAD src0_sel:DWORD src1_sel:WORD_1
	v_or_b32_sdwa v10, v10, v12 dst_sel:DWORD dst_unused:UNUSED_PAD src0_sel:DWORD src1_sel:WORD_1
	ds_write_b64 v132, v[10:11] offset:4512
	v_mov_b32_e32 v10, v120
	v_mov_b32_e32 v11, v121
	v_mov_b32_e32 v12, v122
	v_mov_b32_e32 v13, v123
	v_mov_b32_e32 v15, v6
	v_mov_b32_e32 v6, v9
	v_mov_b32_e32 v14, v8
	v_pk_mul_f32 v[6:7], v[6:7], v[4:5] op_sel_hi:[1,0]
	v_pk_mul_f32 v[14:15], v[14:15], v[4:5] op_sel_hi:[1,0]
	v_mov_b32_e32 v17, v12
	v_mov_b32_e32 v12, v11
	v_mov_b32_e32 v16, v10
	v_pk_mul_f32 v[6:7], v[12:13], v[6:7]
	v_pk_mul_f32 v[14:15], v[16:17], v[14:15]
	v_and_b32_sdwa v9, v7, v213 dst_sel:DWORD dst_unused:UNUSED_PAD src0_sel:WORD_1 src1_sel:DWORD
	v_and_b32_sdwa v10, v6, v213 dst_sel:DWORD dst_unused:UNUSED_PAD src0_sel:WORD_1 src1_sel:DWORD
	v_and_b32_sdwa v5, v15, v213 dst_sel:DWORD dst_unused:UNUSED_PAD src0_sel:WORD_1 src1_sel:DWORD
	v_and_b32_sdwa v8, v14, v213 dst_sel:DWORD dst_unused:UNUSED_PAD src0_sel:WORD_1 src1_sel:DWORD
	v_add3_u32 v7, v7, v9, s76
	v_add3_u32 v6, v6, v10, s76
	v_add3_u32 v8, v14, v8, s76
	v_add3_u32 v5, v15, v5, s76
	v_and_b32_e32 v7, 0xffff0000, v7
	v_and_b32_e32 v6, 0xffff0000, v6
	v_or_b32_sdwa v7, v7, v5 dst_sel:DWORD dst_unused:UNUSED_PAD src0_sel:DWORD src1_sel:WORD_1
	v_or_b32_sdwa v6, v6, v8 dst_sel:DWORD dst_unused:UNUSED_PAD src0_sel:DWORD src1_sel:WORD_1
	ds_write_b64 v132, v[6:7] offset:4544
	v_mov_b32_e32 v6, v124
	v_mov_b32_e32 v7, v125
	v_mov_b32_e32 v8, v126
	v_mov_b32_e32 v9, v127
	v_mov_b32_e32 v11, v0
	v_mov_b32_e32 v0, v3
	v_mov_b32_e32 v10, v2
	v_pk_mul_f32 v[0:1], v[0:1], v[4:5] op_sel_hi:[1,0]
	v_pk_mul_f32 v[10:11], v[10:11], v[4:5] op_sel_hi:[1,0]
	v_mov_b32_e32 v13, v8
	v_mov_b32_e32 v8, v7
	v_mov_b32_e32 v12, v6
	v_pk_mul_f32 v[0:1], v[8:9], v[0:1]
	v_pk_mul_f32 v[10:11], v[12:13], v[10:11]
	v_and_b32_sdwa v4, v1, v213 dst_sel:DWORD dst_unused:UNUSED_PAD src0_sel:WORD_1 src1_sel:DWORD
	v_and_b32_sdwa v5, v0, v213 dst_sel:DWORD dst_unused:UNUSED_PAD src0_sel:WORD_1 src1_sel:DWORD
	v_and_b32_sdwa v2, v11, v213 dst_sel:DWORD dst_unused:UNUSED_PAD src0_sel:WORD_1 src1_sel:DWORD
	v_and_b32_sdwa v3, v10, v213 dst_sel:DWORD dst_unused:UNUSED_PAD src0_sel:WORD_1 src1_sel:DWORD
	v_add3_u32 v1, v1, v4, s76
	v_add3_u32 v0, v0, v5, s76
	v_add3_u32 v3, v10, v3, s76
	v_add3_u32 v2, v11, v2, s76
	v_and_b32_e32 v1, 0xffff0000, v1
	v_and_b32_e32 v0, 0xffff0000, v0
	v_or_b32_sdwa v1, v1, v2 dst_sel:DWORD dst_unused:UNUSED_PAD src0_sel:DWORD src1_sel:WORD_1
	v_or_b32_sdwa v0, v0, v3 dst_sel:DWORD dst_unused:UNUSED_PAD src0_sel:DWORD src1_sel:WORD_1
	ds_write_b64 v132, v[0:1] offset:4576
	s_waitcnt lgkmcnt(0)
	ds_read_b128 v[96:99], v133
	ds_read_b128 v[100:103], v133 offset:1088
	ds_read_b128 v[104:107], v133 offset:2176
	ds_read_b128 v[108:111], v133 offset:3264
	ds_read_b128 v[112:115], v133 offset:4352
	ds_read_b128 v[116:119], v133 offset:5440
	ds_read_b128 v[120:123], v133 offset:6528
	ds_read_b128 v[124:127], v133 offset:7616
	v_mov_b32_e32 v136, 0x4000
	v_mov_b32_e32 v137, 0
	s_waitcnt lgkmcnt(7)
	global_store_dwordx4 v[130:131], v[96:99], off
	v_lshl_add_u64 v[130:131], v[130:131], 0, v[136:137]
	s_waitcnt lgkmcnt(6)
	global_store_dwordx4 v[130:131], v[100:103], off
	v_lshl_add_u64 v[130:131], v[130:131], 0, v[136:137]
	s_waitcnt lgkmcnt(5)
	global_store_dwordx4 v[130:131], v[104:107], off
	v_lshl_add_u64 v[130:131], v[130:131], 0, v[136:137]
	s_waitcnt lgkmcnt(4)
	global_store_dwordx4 v[130:131], v[108:111], off
	v_lshl_add_u64 v[130:131], v[130:131], 0, v[136:137]
	s_waitcnt lgkmcnt(3)
	global_store_dwordx4 v[130:131], v[112:115], off
	v_lshl_add_u64 v[130:131], v[130:131], 0, v[136:137]
	s_waitcnt lgkmcnt(2)
	global_store_dwordx4 v[130:131], v[116:119], off
	v_lshl_add_u64 v[130:131], v[130:131], 0, v[136:137]
	s_waitcnt lgkmcnt(1)
	global_store_dwordx4 v[130:131], v[120:123], off
	v_lshl_add_u64 v[130:131], v[130:131], 0, v[136:137]
	s_waitcnt lgkmcnt(0)
	global_store_dwordx4 v[130:131], v[124:127], off
	s_setprio 0
	s_cbranch_vccnz .LBB0_577

; __global__ void __launch_bounds__(NWAVES * 64, 2) hybrid_fwd(Args args) {
;     ...
;                     const int n = g < 128 ? 1 : 3, w = g - 128;
;                     for (int i = 0; i < n; ++i) {
;                         const int task = g < 128 ? t12(g) : (i < 2 ? t12(128 + 2 * w + i) : (w < 64 ? w * 8 + 1 : (w - 64) * 8));
;                         attn_wg_task(F, l, task); }
.LBB0_521:
	v_readfirstlane_b32 s100, v212
	s_cmp_lt_u32 s100, 0x100
	s_cbranch_scc1 .Lattn_prio_0
	s_setprio 2

; __device__ __forceinline__ float rq_sum(float v) { v += __shfl_xor(v, 16); v += __shfl_xor(v, 32); return v; }
; __device__ __forceinline__ float frsq(float x) { return __builtin_amdgcn_rsqf(x); }
; __device__ __forceinline__ void attn_wg_task(const Frame& F, int l, int task) {
;     ...
;         __syncthreads();
;     }
;     ...
; #pragma unroll
;     for (int qb = 0; qb < 2; ++qb) {
;         const int tq = tq0 + qb * 16;
;         const float inv = 1.0f / rq_sum(l_run[qb]);
;         float ss = 0.f;
; #pragma unroll
;         for (int db = 0; db < 8; ++db) { O[qb][db] *= inv; ss += (O[qb][db][0] * O[qb][db][0] + O[qb][db][1] * O[qb][db][1]) + (O[qb][db][2] * O[qb][db][2] + O[qb][db][3] * O[qb][db][3]); }
;         const float rstd = frsq(rq_sum(ss) * (1.f / HD) + EPS);
.LBB0_549:
	ds_bpermute_b32 v64, v202, v151
	v_lshl_or_b32 v82, v204, 2, s19
	v_readlane_b32 s2, v251, 53
	v_readlane_b32 s3, v251, 54
	s_waitcnt lgkmcnt(0)
	v_add_f32_e32 v64, v151, v64
	ds_bpermute_b32 v65, v203, v64
	s_barrier
	s_waitcnt lgkmcnt(0)
	v_lshlrev_b32_e32 v184, 1, v82
	s_add_i32 s18, s18, s87
	v_add_f32_e32 v64, v64, v65
	v_div_scale_f32 v65, s[0:1], v64, v64, 1.0
	v_rcp_f32_e32 v66, v65
	s_nop 0
	v_fma_f32 v67, -v65, v66, 1.0
	v_fmac_f32_e32 v66, v67, v66
	v_div_scale_f32 v67, vcc, 1.0, v64, 1.0
	v_mul_f32_e32 v68, v67, v66
	v_fma_f32 v69, -v65, v68, v67
	v_fmac_f32_e32 v68, v69, v66
	v_fma_f32 v65, -v65, v68, v67
	v_div_fmas_f32 v65, v65, v66, v68
	v_div_fixup_f32 v84, v65, v64, 1.0
	v_pk_mul_f32 v[80:81], v[32:33], v[84:85] op_sel_hi:[1,0]
	v_pk_mul_f32 v[76:77], v[36:37], v[84:85] op_sel_hi:[1,0]
	v_pk_mul_f32 v[78:79], v[34:35], v[84:85] op_sel_hi:[1,0]
	v_pk_mul_f32 v[74:75], v[38:39], v[84:85] op_sel_hi:[1,0]
	v_mov_b32_e32 v34, v81
	v_mov_b32_e32 v35, v77
	v_mov_b32_e32 v32, v80
	v_mov_b32_e32 v33, v76
	v_pk_mul_f32 v[34:35], v[34:35], v[34:35]
	v_mov_b32_e32 v36, v79
	v_mov_b32_e32 v37, v75
	v_pk_fma_f32 v[32:33], v[32:33], v[32:33], v[34:35]
	v_mov_b32_e32 v34, v78
	v_mov_b32_e32 v35, v74
	v_pk_mul_f32 v[36:37], v[36:37], v[36:37]
	v_pk_mul_f32 v[72:73], v[40:41], v[84:85] op_sel_hi:[1,0]
	v_pk_fma_f32 v[34:35], v[34:35], v[34:35], v[36:37]
	v_pk_mul_f32 v[70:71], v[42:43], v[84:85] op_sel_hi:[1,0]
	v_pk_add_f32 v[32:33], v[32:33], v[34:35]
	v_pk_mul_f32 v[34:35], v[70:71], v[70:71]
	v_pk_add_f32 v[32:33], v[32:33], v[32:33] op_sel_hi:[0,1]
	v_pk_mul_f32 v[36:37], v[72:73], v[72:73]
	v_pk_mul_f32 v[68:69], v[44:45], v[84:85] op_sel_hi:[1,0]
	v_pk_mov_b32 v[38:39], v[36:37], v[34:35] op_sel:[1,0]
	v_mov_b32_e32 v37, v35
	v_pk_mul_f32 v[66:67], v[46:47], v[84:85] op_sel_hi:[1,0]
	v_mul_f32_e32 v32, v68, v68
	v_pk_add_f32 v[34:35], v[38:39], v[36:37]
	v_pk_fma_f32 v[36:37], v[68:69], v[68:69], v[32:33] op_sel_hi:[1,1,0]
	v_mul_f32_e32 v32, v66, v66
	v_pk_add_f32 v[34:35], v[34:35], v[34:35] op_sel_hi:[0,1]
	v_pk_fma_f32 v[38:39], v[66:67], v[66:67], v[32:33] op_sel_hi:[1,1,0]
	v_pk_mul_f32 v[50:51], v[50:51], v[84:85] op_sel_hi:[1,0]
	v_pk_mul_f32 v[64:65], v[48:49], v[84:85] op_sel_hi:[1,0]
	v_mul_f32_e32 v34, v50, v50
	v_mul_f32_e32 v36, v64, v64
	v_mul_f32_e32 v38, v65, v65
	v_mul_f32_e32 v32, v51, v51
	v_pk_add_f32 v[36:37], v[36:37], v[38:39]
	v_pk_add_f32 v[32:33], v[34:35], v[32:33]
	v_pk_mul_f32 v[48:49], v[52:53], v[84:85] op_sel_hi:[1,0]
	v_pk_add_f32 v[32:33], v[36:37], v[32:33]
	v_pk_mul_f32 v[46:47], v[54:55], v[84:85] op_sel_hi:[1,0]
	v_pk_add_f32 v[32:33], v[32:33], v[32:33] op_sel_hi:[0,1]
	v_pk_mul_f32 v[34:35], v[46:47], v[46:47]
	v_pk_mul_f32 v[36:37], v[48:49], v[48:49]
	v_pk_mul_f32 v[44:45], v[56:57], v[84:85] op_sel_hi:[1,0]
	v_pk_mov_b32 v[38:39], v[36:37], v[34:35] op_sel:[1,0]
	v_mov_b32_e32 v37, v35
	v_pk_mul_f32 v[42:43], v[58:59], v[84:85] op_sel_hi:[1,0]
	v_mul_f32_e32 v32, v44, v44
	v_pk_add_f32 v[34:35], v[38:39], v[36:37]
	v_pk_fma_f32 v[40:41], v[44:45], v[44:45], v[32:33] op_sel_hi:[1,1,0]
	v_mul_f32_e32 v32, v42, v42
	v_pk_add_f32 v[34:35], v[34:35], v[34:35] op_sel_hi:[0,1]
	v_pk_fma_f32 v[52:53], v[42:43], v[42:43], v[32:33] op_sel_hi:[1,1,0]
	v_pk_mul_f32 v[36:37], v[62:63], v[84:85] op_sel_hi:[1,0]
	v_pk_mul_f32 v[38:39], v[60:61], v[84:85] op_sel_hi:[1,0]
	v_mul_f32_e32 v34, v36, v36
	v_mul_f32_e32 v40, v38, v38
	v_mul_f32_e32 v52, v39, v39
	v_mul_f32_e32 v32, v37, v37
	v_pk_add_f32 v[40:41], v[40:41], v[52:53]
	v_pk_add_f32 v[32:33], v[34:35], v[32:33]
	v_lshlrev_b32_e32 v54, 2, v82
	global_load_dwordx4 v[96:99], v54, s[42:43]
	global_load_dwordx4 v[100:103], v54, s[42:43] offset:64
	global_load_dwordx4 v[104:107], v54, s[42:43] offset:128
	global_load_dwordx4 v[108:111], v54, s[42:43] offset:192
	global_load_dwordx4 v[112:115], v54, s[42:43] offset:256
	global_load_dwordx4 v[116:119], v54, s[42:43] offset:320
	global_load_dwordx4 v[120:123], v54, s[42:43] offset:384
	global_load_dwordx4 v[124:127], v54, s[42:43] offset:448
	v_pk_add_f32 v[32:33], v[40:41], v[32:33]
	v_mov_b32_e32 v56, v80
	v_add_f32_e32 v32, v32, v33
	ds_bpermute_b32 v33, v202, v32
	v_mov_b32_e32 v57, v78
	v_mov_b32_e32 v78, v81
	s_waitcnt lgkmcnt(0)
	v_add_f32_e32 v32, v32, v33
	ds_bpermute_b32 v33, v203, v32
	s_waitcnt lgkmcnt(0)
	v_add_f32_e32 v32, v32, v33
	v_fmamk_f32 v32, v32, 0x3c000000, v214
	v_rsq_f32_e32 v40, v32
	v_lshlrev_b64 v[32:33], 12, v[152:153]
	v_lshl_add_u64 v[52:53], s[2:3], 0, v[32:33]
	s_waitcnt vmcnt(0)
; __device__ __forceinline__ unsigned pk2(float lo, float hi) { return f2bf(lo) | (f2bf(hi) << 16); }
; __device__ __forceinline__ float rq_sum(float v) { v += __shfl_xor(v, 16); v += __shfl_xor(v, 32); return v; }
; __device__ __forceinline__ float frsq(float x) { return __builtin_amdgcn_rsqf(x); }
; __device__ __forceinline__ void attn_wg_task(const Frame& F, int l, int task) {
;     ...
;         const float rstd = frsq(rq_sum(ss) * (1.f / HD) + EPS);
; #pragma unroll
;         for (int db = 0; db < 8; ++db) {
;             const int d0 = h * HD + db * 16 + rq * 4;
;             const f32x4 g4 = ld_f4(F.attn_g + l * 1024 + d0);
;             u32x2 o; o.x = pk2(O[qb][db][0] * rstd * g4[0], O[qb][db][1] * rstd * g4[1]); o.y = pk2(O[qb][db][2] * rstd * g4[2], O[qb][db][3] * rstd * g4[3]);
;             st_u2(MIX + (size_t)tq * D + d0, o);
	v_mov_b32_e32 v32, v96
	v_mov_b32_e32 v33, v97
	v_mov_b32_e32 v34, v98
	v_mov_b32_e32 v35, v99
	v_pk_mul_f32 v[56:57], v[56:57], v[40:41] op_sel_hi:[1,0]
	v_mov_b32_e32 v58, v32
	v_mov_b32_e32 v59, v34
	v_pk_mul_f32 v[56:57], v[58:59], v[56:57]
	v_pk_mul_f32 v[58:59], v[78:79], v[40:41] op_sel_hi:[1,0]
	v_mov_b32_e32 v34, v33
	v_pk_mul_f32 v[32:33], v[34:35], v[58:59]
	v_and_b32_sdwa v35, v56, v213 dst_sel:DWORD dst_unused:UNUSED_PAD src0_sel:WORD_1 src1_sel:DWORD
	v_add3_u32 v41, v56, v35, s76
	v_and_b32_sdwa v35, v33, v213 dst_sel:DWORD dst_unused:UNUSED_PAD src0_sel:WORD_1 src1_sel:DWORD
	v_and_b32_sdwa v55, v32, v213 dst_sel:DWORD dst_unused:UNUSED_PAD src0_sel:WORD_1 src1_sel:DWORD
	v_and_b32_sdwa v34, v57, v213 dst_sel:DWORD dst_unused:UNUSED_PAD src0_sel:WORD_1 src1_sel:DWORD
	v_add3_u32 v33, v33, v35, s76
	v_add3_u32 v32, v32, v55, s76
	v_add3_u32 v34, v57, v34, s76
	v_and_b32_e32 v33, 0xffff0000, v33
	v_and_b32_e32 v32, 0xffff0000, v32
	v_or_b32_sdwa v35, v33, v34 dst_sel:DWORD dst_unused:UNUSED_PAD src0_sel:DWORD src1_sel:WORD_1
	v_or_b32_sdwa v34, v32, v41 dst_sel:DWORD dst_unused:UNUSED_PAD src0_sel:DWORD src1_sel:WORD_1
	v_lshl_add_u64 v[32:33], v[52:53], 0, v[184:185]
	v_and_b32_e32 v128, 15, v211
	v_lshrrev_b32_e32 v129, 4, v211
	v_lshrrev_b32_e32 v134, 6, v212
	v_mul_u32_u24_e32 v134, 0x2200, v134
	v_add_u32_e32 v134, v229, v134
	v_lshlrev_b32_e32 v135, 3, v129
	v_sub_u32_e32 v132, v134, v135
	v_lshlrev_b32_e32 v135, 8, v129
	v_add_u32_e32 v133, v134, v135
	v_lshlrev_b32_e32 v135, 8, v128
	v_sub_u32_e32 v133, v133, v135
	v_mul_u32_u24_e32 v135, 0xff8, v129
	v_mul_u32_u24_e32 v136, 0xff0, v128
	v_sub_u32_e32 v136, v135, v136
	v_ashrrev_i32_e32 v137, 31, v136
	v_lshl_add_u64 v[130:131], v[32:33], 0, v[136:137]
	ds_write_b64 v132, v[34:35]
	v_mov_b32_e32 v56, v100
	v_mov_b32_e32 v57, v101
	v_mov_b32_e32 v58, v102
	v_mov_b32_e32 v59, v103
	v_mov_b32_e32 v34, v76
	v_mov_b32_e32 v35, v74
	v_pk_mul_f32 v[34:35], v[34:35], v[40:41] op_sel_hi:[1,0]
	v_mov_b32_e32 v74, v77
	v_mov_b32_e32 v52, v56
	v_mov_b32_e32 v53, v58
	v_pk_mul_f32 v[34:35], v[52:53], v[34:35]
	v_pk_mul_f32 v[52:53], v[74:75], v[40:41] op_sel_hi:[1,0]
	v_mov_b32_e32 v58, v57
	v_pk_mul_f32 v[52:53], v[58:59], v[52:53]
	v_and_b32_sdwa v41, v35, v213 dst_sel:DWORD dst_unused:UNUSED_PAD src0_sel:WORD_1 src1_sel:DWORD
	v_and_b32_sdwa v55, v34, v213 dst_sel:DWORD dst_unused:UNUSED_PAD src0_sel:WORD_1 src1_sel:DWORD
	v_add3_u32 v34, v34, v55, s76
	v_add3_u32 v35, v35, v41, s76
	v_and_b32_sdwa v41, v53, v213 dst_sel:DWORD dst_unused:UNUSED_PAD src0_sel:WORD_1 src1_sel:DWORD
	v_and_b32_sdwa v55, v52, v213 dst_sel:DWORD dst_unused:UNUSED_PAD src0_sel:WORD_1 src1_sel:DWORD
	v_add3_u32 v41, v53, v41, s76
	v_add3_u32 v52, v52, v55, s76
	v_and_b32_e32 v41, 0xffff0000, v41
	v_and_b32_e32 v52, 0xffff0000, v52
	v_or_b32_sdwa v35, v41, v35 dst_sel:DWORD dst_unused:UNUSED_PAD src0_sel:DWORD src1_sel:WORD_1
	v_or_b32_sdwa v34, v52, v34 dst_sel:DWORD dst_unused:UNUSED_PAD src0_sel:DWORD src1_sel:WORD_1
	ds_write_b64 v132, v[34:35] offset:32
	v_mov_b32_e32 v56, v104
	v_mov_b32_e32 v57, v105
	v_mov_b32_e32 v58, v106
	v_mov_b32_e32 v59, v107
	v_mov_b32_e32 v34, v72
	v_mov_b32_e32 v35, v70
	v_pk_mul_f32 v[34:35], v[34:35], v[40:41] op_sel_hi:[1,0]
	v_mov_b32_e32 v70, v73
	v_mov_b32_e32 v52, v56
	v_mov_b32_e32 v53, v58
	v_pk_mul_f32 v[34:35], v[52:53], v[34:35]
	v_pk_mul_f32 v[52:53], v[70:71], v[40:41] op_sel_hi:[1,0]
	v_mov_b32_e32 v58, v57
	v_pk_mul_f32 v[52:53], v[58:59], v[52:53]
	v_and_b32_sdwa v41, v35, v213 dst_sel:DWORD dst_unused:UNUSED_PAD src0_sel:WORD_1 src1_sel:DWORD
	v_and_b32_sdwa v55, v34, v213 dst_sel:DWORD dst_unused:UNUSED_PAD src0_sel:WORD_1 src1_sel:DWORD
	v_add3_u32 v34, v34, v55, s76
	v_add3_u32 v35, v35, v41, s76
	v_and_b32_sdwa v41, v53, v213 dst_sel:DWORD dst_unused:UNUSED_PAD src0_sel:WORD_1 src1_sel:DWORD
	v_and_b32_sdwa v55, v52, v213 dst_sel:DWORD dst_unused:UNUSED_PAD src0_sel:WORD_1 src1_sel:DWORD
	v_add3_u32 v41, v53, v41, s76
	v_add3_u32 v52, v52, v55, s76
	v_and_b32_e32 v41, 0xffff0000, v41
	v_and_b32_e32 v52, 0xffff0000, v52
	v_or_b32_sdwa v35, v41, v35 dst_sel:DWORD dst_unused:UNUSED_PAD src0_sel:DWORD src1_sel:WORD_1
	v_or_b32_sdwa v34, v52, v34 dst_sel:DWORD dst_unused:UNUSED_PAD src0_sel:DWORD src1_sel:WORD_1
	ds_write_b64 v132, v[34:35] offset:64
	v_mov_b32_e32 v56, v108
	v_mov_b32_e32 v57, v109
	v_mov_b32_e32 v58, v110
	v_mov_b32_e32 v59, v111
	v_mov_b32_e32 v34, v68
	v_mov_b32_e32 v35, v66
	v_pk_mul_f32 v[34:35], v[34:35], v[40:41] op_sel_hi:[1,0]
	v_mov_b32_e32 v66, v69
	v_mov_b32_e32 v52, v56
	v_mov_b32_e32 v53, v58
	v_pk_mul_f32 v[34:35], v[52:53], v[34:35]
	v_pk_mul_f32 v[52:53], v[66:67], v[40:41] op_sel_hi:[1,0]
	v_mov_b32_e32 v58, v57
	v_pk_mul_f32 v[52:53], v[58:59], v[52:53]
	v_and_b32_sdwa v41, v35, v213 dst_sel:DWORD dst_unused:UNUSED_PAD src0_sel:WORD_1 src1_sel:DWORD
	v_and_b32_sdwa v55, v34, v213 dst_sel:DWORD dst_unused:UNUSED_PAD src0_sel:WORD_1 src1_sel:DWORD
	v_add3_u32 v34, v34, v55, s76
	v_add3_u32 v35, v35, v41, s76
	v_and_b32_sdwa v41, v53, v213 dst_sel:DWORD dst_unused:UNUSED_PAD src0_sel:WORD_1 src1_sel:DWORD
	v_and_b32_sdwa v55, v52, v213 dst_sel:DWORD dst_unused:UNUSED_PAD src0_sel:WORD_1 src1_sel:DWORD
	v_add3_u32 v41, v53, v41, s76
	v_add3_u32 v52, v52, v55, s76
	v_and_b32_e32 v41, 0xffff0000, v41
	v_and_b32_e32 v52, 0xffff0000, v52
	v_or_b32_sdwa v35, v41, v35 dst_sel:DWORD dst_unused:UNUSED_PAD src0_sel:DWORD src1_sel:WORD_1
	v_or_b32_sdwa v34, v52, v34 dst_sel:DWORD dst_unused:UNUSED_PAD src0_sel:DWORD src1_sel:WORD_1
	ds_write_b64 v132, v[34:35] offset:96
	v_mov_b32_e32 v56, v112
	v_mov_b32_e32 v57, v113
; __device__ __forceinline__ unsigned pk2(float lo, float hi) { return f2bf(lo) | (f2bf(hi) << 16); }
; __device__ __forceinline__ float rq_sum(float v) { v += __shfl_xor(v, 16); v += __shfl_xor(v, 32); return v; }
; __device__ __forceinline__ void attn_wg_task(const Frame& F, int l, int task) {
;     ...
;         const float inv = 1.0f / rq_sum(l_run[qb]);
;     ...
;         for (int db = 0; db < 8; ++db) {
;             const int d0 = h * HD + db * 16 + rq * 4;
;             const f32x4 g4 = ld_f4(F.attn_g + l * 1024 + d0);
;             u32x2 o; o.x = pk2(O[qb][db][0] * rstd * g4[0], O[qb][db][1] * rstd * g4[1]); o.y = pk2(O[qb][db][2] * rstd * g4[2], O[qb][db][3] * rstd * g4[3]);
;             st_u2(MIX + (size_t)tq * D + d0, o);
;         }
	v_mov_b32_e32 v58, v114
	v_mov_b32_e32 v59, v115
	v_mov_b32_e32 v34, v64
	v_mov_b32_e32 v35, v50
	v_pk_mul_f32 v[34:35], v[34:35], v[40:41] op_sel_hi:[1,0]
	v_mov_b32_e32 v50, v65
	v_pk_mul_f32 v[50:51], v[50:51], v[40:41] op_sel_hi:[1,0]
	v_mov_b32_e32 v52, v56
	v_mov_b32_e32 v53, v58
	v_pk_mul_f32 v[34:35], v[52:53], v[34:35]
	v_mov_b32_e32 v58, v57
	v_pk_mul_f32 v[50:51], v[58:59], v[50:51]
	v_and_b32_sdwa v41, v35, v213 dst_sel:DWORD dst_unused:UNUSED_PAD src0_sel:WORD_1 src1_sel:DWORD
	v_and_b32_sdwa v52, v34, v213 dst_sel:DWORD dst_unused:UNUSED_PAD src0_sel:WORD_1 src1_sel:DWORD
	v_add3_u32 v34, v34, v52, s76
	v_add3_u32 v35, v35, v41, s76
	v_and_b32_sdwa v41, v51, v213 dst_sel:DWORD dst_unused:UNUSED_PAD src0_sel:WORD_1 src1_sel:DWORD
	v_and_b32_sdwa v52, v50, v213 dst_sel:DWORD dst_unused:UNUSED_PAD src0_sel:WORD_1 src1_sel:DWORD
	v_add3_u32 v41, v51, v41, s76
	v_add3_u32 v50, v50, v52, s76
	v_and_b32_e32 v41, 0xffff0000, v41
	v_and_b32_e32 v50, 0xffff0000, v50
	v_or_b32_sdwa v35, v41, v35 dst_sel:DWORD dst_unused:UNUSED_PAD src0_sel:DWORD src1_sel:WORD_1
	v_or_b32_sdwa v34, v50, v34 dst_sel:DWORD dst_unused:UNUSED_PAD src0_sel:DWORD src1_sel:WORD_1
	ds_write_b64 v132, v[34:35] offset:128
	v_mov_b32_e32 v50, v116
	v_mov_b32_e32 v51, v117
	v_mov_b32_e32 v52, v118
	v_mov_b32_e32 v53, v119
	v_mov_b32_e32 v34, v48
	v_mov_b32_e32 v35, v46
	v_pk_mul_f32 v[34:35], v[34:35], v[40:41] op_sel_hi:[1,0]
	v_mov_b32_e32 v46, v49
	v_pk_mul_f32 v[46:47], v[46:47], v[40:41] op_sel_hi:[1,0]
	v_mov_b32_e32 v56, v50
	v_mov_b32_e32 v57, v52
	v_pk_mul_f32 v[34:35], v[56:57], v[34:35]
	v_mov_b32_e32 v52, v51
	v_pk_mul_f32 v[46:47], v[52:53], v[46:47]
	v_and_b32_sdwa v41, v35, v213 dst_sel:DWORD dst_unused:UNUSED_PAD src0_sel:WORD_1 src1_sel:DWORD
	v_and_b32_sdwa v48, v34, v213 dst_sel:DWORD dst_unused:UNUSED_PAD src0_sel:WORD_1 src1_sel:DWORD
	v_add3_u32 v34, v34, v48, s76
	v_add3_u32 v35, v35, v41, s76
	v_and_b32_sdwa v41, v47, v213 dst_sel:DWORD dst_unused:UNUSED_PAD src0_sel:WORD_1 src1_sel:DWORD
	v_and_b32_sdwa v48, v46, v213 dst_sel:DWORD dst_unused:UNUSED_PAD src0_sel:WORD_1 src1_sel:DWORD
	v_add3_u32 v41, v47, v41, s76
	v_add3_u32 v46, v46, v48, s76
	v_and_b32_e32 v41, 0xffff0000, v41
	v_and_b32_e32 v46, 0xffff0000, v46
	v_or_b32_sdwa v35, v41, v35 dst_sel:DWORD dst_unused:UNUSED_PAD src0_sel:DWORD src1_sel:WORD_1
	v_or_b32_sdwa v34, v46, v34 dst_sel:DWORD dst_unused:UNUSED_PAD src0_sel:DWORD src1_sel:WORD_1
	ds_write_b64 v132, v[34:35] offset:160
	v_mov_b32_e32 v46, v120
	v_mov_b32_e32 v47, v121
	v_mov_b32_e32 v48, v122
	v_mov_b32_e32 v49, v123
	v_mov_b32_e32 v34, v44
	v_mov_b32_e32 v35, v42
	v_pk_mul_f32 v[34:35], v[34:35], v[40:41] op_sel_hi:[1,0]
	v_mov_b32_e32 v42, v45
	v_pk_mul_f32 v[42:43], v[42:43], v[40:41] op_sel_hi:[1,0]
	v_mov_b32_e32 v50, v46
	v_mov_b32_e32 v51, v48
	v_pk_mul_f32 v[34:35], v[50:51], v[34:35]
	v_mov_b32_e32 v48, v47
	v_pk_mul_f32 v[42:43], v[48:49], v[42:43]
	v_and_b32_sdwa v41, v35, v213 dst_sel:DWORD dst_unused:UNUSED_PAD src0_sel:WORD_1 src1_sel:DWORD
	v_and_b32_sdwa v44, v34, v213 dst_sel:DWORD dst_unused:UNUSED_PAD src0_sel:WORD_1 src1_sel:DWORD
	v_add3_u32 v34, v34, v44, s76
	v_add3_u32 v35, v35, v41, s76
	v_and_b32_sdwa v41, v43, v213 dst_sel:DWORD dst_unused:UNUSED_PAD src0_sel:WORD_1 src1_sel:DWORD
	v_and_b32_sdwa v44, v42, v213 dst_sel:DWORD dst_unused:UNUSED_PAD src0_sel:WORD_1 src1_sel:DWORD
	v_add3_u32 v41, v43, v41, s76
	v_add3_u32 v42, v42, v44, s76
	v_and_b32_e32 v41, 0xffff0000, v41
	v_and_b32_e32 v42, 0xffff0000, v42
	v_or_b32_sdwa v35, v41, v35 dst_sel:DWORD dst_unused:UNUSED_PAD src0_sel:DWORD src1_sel:WORD_1
	v_or_b32_sdwa v34, v42, v34 dst_sel:DWORD dst_unused:UNUSED_PAD src0_sel:DWORD src1_sel:WORD_1
	ds_write_b64 v132, v[34:35] offset:192
	v_mov_b32_e32 v42, v124
	v_mov_b32_e32 v43, v125
	v_mov_b32_e32 v44, v126
	v_mov_b32_e32 v45, v127
	v_mov_b32_e32 v34, v38
	v_mov_b32_e32 v35, v36
	v_pk_mul_f32 v[34:35], v[34:35], v[40:41] op_sel_hi:[1,0]
	v_mov_b32_e32 v36, v39
	v_pk_mul_f32 v[36:37], v[36:37], v[40:41] op_sel_hi:[1,0]
	v_mov_b32_e32 v46, v42
	v_mov_b32_e32 v47, v44
	v_pk_mul_f32 v[34:35], v[46:47], v[34:35]
	v_mov_b32_e32 v44, v43
	v_pk_mul_f32 v[36:37], v[44:45], v[36:37]
	v_and_b32_sdwa v38, v35, v213 dst_sel:DWORD dst_unused:UNUSED_PAD src0_sel:WORD_1 src1_sel:DWORD
	v_and_b32_sdwa v39, v34, v213 dst_sel:DWORD dst_unused:UNUSED_PAD src0_sel:WORD_1 src1_sel:DWORD
	v_add3_u32 v34, v34, v39, s76
	v_add3_u32 v35, v35, v38, s76
	v_and_b32_sdwa v38, v37, v213 dst_sel:DWORD dst_unused:UNUSED_PAD src0_sel:WORD_1 src1_sel:DWORD
	v_and_b32_sdwa v39, v36, v213 dst_sel:DWORD dst_unused:UNUSED_PAD src0_sel:WORD_1 src1_sel:DWORD
	v_add3_u32 v37, v37, v38, s76
	v_add3_u32 v36, v36, v39, s76
	v_and_b32_e32 v37, 0xffff0000, v37
	v_and_b32_e32 v36, 0xffff0000, v36
	v_or_b32_sdwa v35, v37, v35 dst_sel:DWORD dst_unused:UNUSED_PAD src0_sel:DWORD src1_sel:WORD_1
	v_or_b32_sdwa v34, v36, v34 dst_sel:DWORD dst_unused:UNUSED_PAD src0_sel:DWORD src1_sel:WORD_1
	ds_write_b64 v132, v[34:35] offset:224
	ds_bpermute_b32 v32, v202, v150
	s_waitcnt lgkmcnt(0)
	v_add_f32_e32 v32, v150, v32
	ds_bpermute_b32 v33, v203, v32
	s_waitcnt lgkmcnt(0)
; __device__ __forceinline__ unsigned pk2(float lo, float hi) { return f2bf(lo) | (f2bf(hi) << 16); }
; __device__ __forceinline__ float rq_sum(float v) { v += __shfl_xor(v, 16); v += __shfl_xor(v, 32); return v; }
; __device__ __forceinline__ float frsq(float x) { return __builtin_amdgcn_rsqf(x); }
; __device__ __forceinline__ void attn_wg_task(const Frame& F, int l, int task) {
;     ...
;         const float inv = 1.0f / rq_sum(l_run[qb]);
;         float ss = 0.f;
; #pragma unroll
;         for (int db = 0; db < 8; ++db) { O[qb][db] *= inv; ss += (O[qb][db][0] * O[qb][db][0] + O[qb][db][1] * O[qb][db][1]) + (O[qb][db][2] * O[qb][db][2] + O[qb][db][3] * O[qb][db][3]); }
;         const float rstd = frsq(rq_sum(ss) * (1.f / HD) + EPS);
; #pragma unroll
;         for (int db = 0; db < 8; ++db) {
;             const int d0 = h * HD + db * 16 + rq * 4;
;             const f32x4 g4 = ld_f4(F.attn_g + l * 1024 + d0);
;             u32x2 o; o.x = pk2(O[qb][db][0] * rstd * g4[0], O[qb][db][1] * rstd * g4[1]); o.y = pk2(O[qb][db][2] * rstd * g4[2], O[qb][db][3] * rstd * g4[3]);
;             st_u2(MIX + (size_t)tq * D + d0, o);
;         }
	v_add_f32_e32 v32, v32, v33
	v_div_scale_f32 v33, s[0:1], v32, v32, 1.0
	v_rcp_f32_e32 v34, v33
	v_readlane_b32 s0, v250, 0
	s_add_i32 s17, s17, s0
	v_readlane_b32 s0, v250, 2
	v_fma_f32 v35, -v33, v34, 1.0
	v_fmac_f32_e32 v34, v35, v34
	v_div_scale_f32 v35, vcc, 1.0, v32, 1.0
	v_mul_f32_e32 v36, v35, v34
	v_fma_f32 v37, -v33, v36, v35
	v_fmac_f32_e32 v36, v37, v34
	v_fma_f32 v33, -v33, v36, v35
	v_div_fmas_f32 v33, v33, v34, v36
	v_div_fixup_f32 v48, v33, v32, 1.0
	v_pk_mul_f32 v[46:47], v[4:5], v[48:49] op_sel_hi:[1,0]
	v_pk_mul_f32 v[42:43], v[8:9], v[48:49] op_sel_hi:[1,0]
	v_pk_mul_f32 v[44:45], v[6:7], v[48:49] op_sel_hi:[1,0]
	v_pk_mul_f32 v[36:37], v[10:11], v[48:49] op_sel_hi:[1,0]
	v_mov_b32_e32 v6, v47
	v_mov_b32_e32 v7, v43
	v_mov_b32_e32 v4, v46
	v_mov_b32_e32 v5, v42
	v_pk_mul_f32 v[6:7], v[6:7], v[6:7]
	v_mov_b32_e32 v8, v45
	v_mov_b32_e32 v9, v37
	v_pk_fma_f32 v[4:5], v[4:5], v[4:5], v[6:7]
	v_mov_b32_e32 v6, v44
	v_mov_b32_e32 v7, v36
	v_pk_mul_f32 v[8:9], v[8:9], v[8:9]
	v_pk_mul_f32 v[40:41], v[0:1], v[48:49] op_sel_hi:[1,0]
	v_pk_mul_f32 v[38:39], v[2:3], v[48:49] op_sel_hi:[1,0]
	v_pk_fma_f32 v[6:7], v[6:7], v[6:7], v[8:9]
	v_pk_mul_f32 v[0:1], v[38:39], v[38:39]
	v_pk_mul_f32 v[2:3], v[40:41], v[40:41]
	v_pk_add_f32 v[4:5], v[4:5], v[6:7]
	v_pk_mov_b32 v[6:7], v[2:3], v[0:1] op_sel:[1,0]
	v_mov_b32_e32 v3, v1
	v_pk_add_f32 v[0:1], v[6:7], v[2:3]
	v_pk_mul_f32 v[34:35], v[12:13], v[48:49] op_sel_hi:[1,0]
	v_pk_add_f32 v[0:1], v[0:1], v[0:1] op_sel_hi:[0,1]
	v_pk_mul_f32 v[32:33], v[14:15], v[48:49] op_sel_hi:[1,0]
	v_mul_f32_e32 v0, v34, v34
	v_pk_fma_f32 v[2:3], v[34:35], v[34:35], v[0:1] op_sel_hi:[1,1,0]
	v_mul_f32_e32 v0, v32, v32
	v_pk_add_f32 v[4:5], v[4:5], v[4:5] op_sel_hi:[0,1]
	v_pk_fma_f32 v[6:7], v[32:33], v[32:33], v[0:1] op_sel_hi:[1,1,0]
	v_pk_mul_f32 v[14:15], v[18:19], v[48:49] op_sel_hi:[1,0]
	v_pk_mul_f32 v[16:17], v[16:17], v[48:49] op_sel_hi:[1,0]
	v_mul_f32_e32 v0, v14, v14
	v_mul_f32_e32 v2, v16, v16
	v_mul_f32_e32 v6, v17, v17
	v_mul_f32_e32 v4, v15, v15
	v_pk_add_f32 v[2:3], v[2:3], v[6:7]
	v_pk_add_f32 v[0:1], v[0:1], v[4:5]
	v_pk_mul_f32 v[12:13], v[20:21], v[48:49] op_sel_hi:[1,0]
	v_pk_add_f32 v[0:1], v[2:3], v[0:1]
	v_pk_mul_f32 v[10:11], v[22:23], v[48:49] op_sel_hi:[1,0]
	v_pk_add_f32 v[4:5], v[0:1], v[0:1] op_sel_hi:[0,1]
	v_pk_mul_f32 v[0:1], v[10:11], v[10:11]
	v_pk_mul_f32 v[2:3], v[12:13], v[12:13]
	v_pk_mul_f32 v[8:9], v[24:25], v[48:49] op_sel_hi:[1,0]
	v_pk_mov_b32 v[6:7], v[2:3], v[0:1] op_sel:[1,0]
	v_mov_b32_e32 v3, v1
	v_pk_add_f32 v[0:1], v[6:7], v[2:3]
	v_pk_mul_f32 v[6:7], v[26:27], v[48:49] op_sel_hi:[1,0]
	v_pk_add_f32 v[18:19], v[0:1], v[0:1] op_sel_hi:[0,1]
	v_mul_f32_e32 v0, v8, v8
	v_pk_fma_f32 v[20:21], v[8:9], v[8:9], v[0:1] op_sel_hi:[1,1,0]
	v_mul_f32_e32 v0, v6, v6
	v_pk_fma_f32 v[22:23], v[6:7], v[6:7], v[0:1] op_sel_hi:[1,1,0]
	v_pk_mul_f32 v[0:1], v[30:31], v[48:49] op_sel_hi:[1,0]
	v_pk_mul_f32 v[2:3], v[28:29], v[48:49] op_sel_hi:[1,0]
	v_mul_f32_e32 v18, v0, v0
	v_mul_f32_e32 v20, v2, v2
	v_mul_f32_e32 v22, v3, v3
	v_mul_f32_e32 v4, v1, v1
	v_pk_add_f32 v[20:21], v[20:21], v[22:23]
	v_pk_add_f32 v[4:5], v[18:19], v[4:5]
	v_mov_b32_e32 v24, v46
	v_pk_add_f32 v[4:5], v[20:21], v[4:5]
	v_mov_b32_e32 v20, v96
	v_mov_b32_e32 v21, v97
	v_mov_b32_e32 v22, v98
	v_mov_b32_e32 v23, v99
	v_add_f32_e32 v4, v4, v5
	ds_bpermute_b32 v5, v202, v4
	v_mov_b32_e32 v25, v44
	v_mov_b32_e32 v44, v47
	v_lshlrev_b64 v[18:19], 12, v[148:149]
	v_lshl_add_u64 v[18:19], s[2:3], 0, v[18:19]
	s_waitcnt lgkmcnt(0)
	v_add_f32_e32 v4, v4, v5
	ds_bpermute_b32 v5, v203, v4
	v_lshl_add_u64 v[18:19], v[18:19], 0, v[184:185]
	s_add_i32 s16, s16, s0
	s_cmpk_lt_i32 s18, 0x200
	s_waitcnt lgkmcnt(0)
	v_add_f32_e32 v4, v4, v5
	v_fmamk_f32 v4, v4, 0x3c000000, v214
	v_rsq_f32_e32 v4, v4
	v_mov_b32_e32 v26, v20
	v_pk_mul_f32 v[24:25], v[24:25], v[4:5] op_sel_hi:[1,0]
	v_mov_b32_e32 v27, v22
	v_pk_mul_f32 v[24:25], v[26:27], v[24:25]
	v_pk_mul_f32 v[26:27], v[44:45], v[4:5] op_sel_hi:[1,0]
	v_mov_b32_e32 v22, v21
	v_pk_mul_f32 v[20:21], v[22:23], v[26:27]
	v_and_b32_sdwa v22, v24, v213 dst_sel:DWORD dst_unused:UNUSED_PAD src0_sel:WORD_1 src1_sel:DWORD
	v_add3_u32 v22, v24, v22, s76
	v_and_b32_sdwa v23, v21, v213 dst_sel:DWORD dst_unused:UNUSED_PAD src0_sel:WORD_1 src1_sel:DWORD
	v_and_b32_sdwa v24, v20, v213 dst_sel:DWORD dst_unused:UNUSED_PAD src0_sel:WORD_1 src1_sel:DWORD
	v_and_b32_sdwa v5, v25, v213 dst_sel:DWORD dst_unused:UNUSED_PAD src0_sel:WORD_1 src1_sel:DWORD
	v_add3_u32 v21, v21, v23, s76
	v_add3_u32 v20, v20, v24, s76
	v_add3_u32 v5, v25, v5, s76
	v_and_b32_e32 v21, 0xffff0000, v21
	v_and_b32_e32 v20, 0xffff0000, v20
	v_or_b32_sdwa v21, v21, v5 dst_sel:DWORD dst_unused:UNUSED_PAD src0_sel:DWORD src1_sel:WORD_1
	v_or_b32_sdwa v20, v20, v22 dst_sel:DWORD dst_unused:UNUSED_PAD src0_sel:DWORD src1_sel:WORD_1
	ds_write_b64 v132, v[20:21] offset:4352
	v_mov_b32_e32 v20, v100
	v_mov_b32_e32 v21, v101
	v_mov_b32_e32 v22, v102
	v_mov_b32_e32 v23, v103
	v_mov_b32_e32 v24, v42
	v_mov_b32_e32 v25, v36
	v_pk_mul_f32 v[24:25], v[24:25], v[4:5] op_sel_hi:[1,0]
	v_mov_b32_e32 v36, v43
	v_mov_b32_e32 v26, v20
	v_mov_b32_e32 v27, v22
	v_pk_mul_f32 v[24:25], v[26:27], v[24:25]
	v_pk_mul_f32 v[26:27], v[36:37], v[4:5] op_sel_hi:[1,0]
	v_mov_b32_e32 v22, v21
	v_pk_mul_f32 v[20:21], v[22:23], v[26:27]
	v_and_b32_sdwa v22, v24, v213 dst_sel:DWORD dst_unused:UNUSED_PAD src0_sel:WORD_1 src1_sel:DWORD
	v_add3_u32 v22, v24, v22, s76
	v_and_b32_sdwa v23, v21, v213 dst_sel:DWORD dst_unused:UNUSED_PAD src0_sel:WORD_1 src1_sel:DWORD
	v_and_b32_sdwa v24, v20, v213 dst_sel:DWORD dst_unused:UNUSED_PAD src0_sel:WORD_1 src1_sel:DWORD
; __device__ __forceinline__ unsigned pk2(float lo, float hi) { return f2bf(lo) | (f2bf(hi) << 16); }
; __device__ __forceinline__ void attn_wg_task(const Frame& F, int l, int task) {
;     ...
;         for (int db = 0; db < 8; ++db) {
;             const int d0 = h * HD + db * 16 + rq * 4;
;             const f32x4 g4 = ld_f4(F.attn_g + l * 1024 + d0);
;             u32x2 o; o.x = pk2(O[qb][db][0] * rstd * g4[0], O[qb][db][1] * rstd * g4[1]); o.y = pk2(O[qb][db][2] * rstd * g4[2], O[qb][db][3] * rstd * g4[3]);
;             st_u2(MIX + (size_t)tq * D + d0, o);
;         }
	v_and_b32_sdwa v5, v25, v213 dst_sel:DWORD dst_unused:UNUSED_PAD src0_sel:WORD_1 src1_sel:DWORD
	v_add3_u32 v21, v21, v23, s76
	v_add3_u32 v20, v20, v24, s76
	v_add3_u32 v5, v25, v5, s76
	v_and_b32_e32 v21, 0xffff0000, v21
	v_and_b32_e32 v20, 0xffff0000, v20
	v_or_b32_sdwa v21, v21, v5 dst_sel:DWORD dst_unused:UNUSED_PAD src0_sel:DWORD src1_sel:WORD_1
	v_or_b32_sdwa v20, v20, v22 dst_sel:DWORD dst_unused:UNUSED_PAD src0_sel:DWORD src1_sel:WORD_1
	ds_write_b64 v132, v[20:21] offset:4384
	v_mov_b32_e32 v20, v104
	v_mov_b32_e32 v21, v105
	v_mov_b32_e32 v22, v106
	v_mov_b32_e32 v23, v107
	v_mov_b32_e32 v24, v40
	v_mov_b32_e32 v25, v38
	v_pk_mul_f32 v[24:25], v[24:25], v[4:5] op_sel_hi:[1,0]
	v_mov_b32_e32 v38, v41
	v_mov_b32_e32 v26, v20
	v_mov_b32_e32 v27, v22
	v_pk_mul_f32 v[24:25], v[26:27], v[24:25]
	v_pk_mul_f32 v[26:27], v[38:39], v[4:5] op_sel_hi:[1,0]
	v_mov_b32_e32 v22, v21
	v_pk_mul_f32 v[20:21], v[22:23], v[26:27]
	v_and_b32_sdwa v22, v24, v213 dst_sel:DWORD dst_unused:UNUSED_PAD src0_sel:WORD_1 src1_sel:DWORD
	v_add3_u32 v22, v24, v22, s76
	v_and_b32_sdwa v23, v21, v213 dst_sel:DWORD dst_unused:UNUSED_PAD src0_sel:WORD_1 src1_sel:DWORD
	v_and_b32_sdwa v24, v20, v213 dst_sel:DWORD dst_unused:UNUSED_PAD src0_sel:WORD_1 src1_sel:DWORD
	v_and_b32_sdwa v5, v25, v213 dst_sel:DWORD dst_unused:UNUSED_PAD src0_sel:WORD_1 src1_sel:DWORD
	v_add3_u32 v21, v21, v23, s76
	v_add3_u32 v20, v20, v24, s76
	v_add3_u32 v5, v25, v5, s76
	v_and_b32_e32 v21, 0xffff0000, v21
	v_and_b32_e32 v20, 0xffff0000, v20
	v_or_b32_sdwa v21, v21, v5 dst_sel:DWORD dst_unused:UNUSED_PAD src0_sel:DWORD src1_sel:WORD_1
	v_or_b32_sdwa v20, v20, v22 dst_sel:DWORD dst_unused:UNUSED_PAD src0_sel:DWORD src1_sel:WORD_1
	ds_write_b64 v132, v[20:21] offset:4416
	v_mov_b32_e32 v20, v108
	v_mov_b32_e32 v21, v109
	v_mov_b32_e32 v22, v110
	v_mov_b32_e32 v23, v111
	v_mov_b32_e32 v24, v34
	v_mov_b32_e32 v25, v32
	v_pk_mul_f32 v[24:25], v[24:25], v[4:5] op_sel_hi:[1,0]
	v_mov_b32_e32 v32, v35
	v_mov_b32_e32 v26, v20
	v_mov_b32_e32 v27, v22
	v_pk_mul_f32 v[24:25], v[26:27], v[24:25]
	v_pk_mul_f32 v[26:27], v[32:33], v[4:5] op_sel_hi:[1,0]
	v_mov_b32_e32 v22, v21
	v_pk_mul_f32 v[20:21], v[22:23], v[26:27]
	v_and_b32_sdwa v22, v24, v213 dst_sel:DWORD dst_unused:UNUSED_PAD src0_sel:WORD_1 src1_sel:DWORD
	v_add3_u32 v22, v24, v22, s76
	v_and_b32_sdwa v23, v21, v213 dst_sel:DWORD dst_unused:UNUSED_PAD src0_sel:WORD_1 src1_sel:DWORD
	v_and_b32_sdwa v24, v20, v213 dst_sel:DWORD dst_unused:UNUSED_PAD src0_sel:WORD_1 src1_sel:DWORD
	v_and_b32_sdwa v5, v25, v213 dst_sel:DWORD dst_unused:UNUSED_PAD src0_sel:WORD_1 src1_sel:DWORD
	v_add3_u32 v21, v21, v23, s76
	v_add3_u32 v20, v20, v24, s76
	v_add3_u32 v5, v25, v5, s76
	v_and_b32_e32 v21, 0xffff0000, v21
	v_and_b32_e32 v20, 0xffff0000, v20
	v_or_b32_sdwa v21, v21, v5 dst_sel:DWORD dst_unused:UNUSED_PAD src0_sel:DWORD src1_sel:WORD_1
	v_or_b32_sdwa v20, v20, v22 dst_sel:DWORD dst_unused:UNUSED_PAD src0_sel:DWORD src1_sel:WORD_1
	ds_write_b64 v132, v[20:21] offset:4448
	v_mov_b32_e32 v20, v112
	v_mov_b32_e32 v21, v113
	v_mov_b32_e32 v22, v114
	v_mov_b32_e32 v23, v115
	v_mov_b32_e32 v25, v14
	v_mov_b32_e32 v14, v17
	v_mov_b32_e32 v24, v16
	v_pk_mul_f32 v[14:15], v[14:15], v[4:5] op_sel_hi:[1,0]
	v_pk_mul_f32 v[24:25], v[24:25], v[4:5] op_sel_hi:[1,0]
	v_mov_b32_e32 v27, v22
	v_mov_b32_e32 v22, v21
	v_mov_b32_e32 v26, v20
	v_pk_mul_f32 v[14:15], v[22:23], v[14:15]
	v_pk_mul_f32 v[24:25], v[26:27], v[24:25]
	v_and_b32_sdwa v17, v15, v213 dst_sel:DWORD dst_unused:UNUSED_PAD src0_sel:WORD_1 src1_sel:DWORD
	v_and_b32_sdwa v20, v14, v213 dst_sel:DWORD dst_unused:UNUSED_PAD src0_sel:WORD_1 src1_sel:DWORD
	v_and_b32_sdwa v5, v25, v213 dst_sel:DWORD dst_unused:UNUSED_PAD src0_sel:WORD_1 src1_sel:DWORD
	v_and_b32_sdwa v16, v24, v213 dst_sel:DWORD dst_unused:UNUSED_PAD src0_sel:WORD_1 src1_sel:DWORD
	v_add3_u32 v15, v15, v17, s76
	v_add3_u32 v14, v14, v20, s76
	v_add3_u32 v16, v24, v16, s76
	v_add3_u32 v5, v25, v5, s76
	v_and_b32_e32 v15, 0xffff0000, v15
	v_and_b32_e32 v14, 0xffff0000, v14
	v_or_b32_sdwa v15, v15, v5 dst_sel:DWORD dst_unused:UNUSED_PAD src0_sel:DWORD src1_sel:WORD_1
	v_or_b32_sdwa v14, v14, v16 dst_sel:DWORD dst_unused:UNUSED_PAD src0_sel:DWORD src1_sel:WORD_1
	ds_write_b64 v132, v[14:15] offset:4480
	v_mov_b32_e32 v14, v116
	v_mov_b32_e32 v15, v117
	v_mov_b32_e32 v16, v118
	v_mov_b32_e32 v17, v119
	v_mov_b32_e32 v21, v10
	v_mov_b32_e32 v10, v13
	v_mov_b32_e32 v20, v12
	v_pk_mul_f32 v[10:11], v[10:11], v[4:5] op_sel_hi:[1,0]
	v_pk_mul_f32 v[20:21], v[20:21], v[4:5] op_sel_hi:[1,0]
	v_mov_b32_e32 v23, v16
	v_mov_b32_e32 v16, v15
	v_mov_b32_e32 v22, v14
	v_pk_mul_f32 v[10:11], v[16:17], v[10:11]
; __device__ __forceinline__ unsigned pk2(float lo, float hi) { return f2bf(lo) | (f2bf(hi) << 16); }
; __device__ __forceinline__ void attn_wg_task(const Frame& F, int l, int task) {
;     ...
;         for (int db = 0; db < 8; ++db) {
;             const int d0 = h * HD + db * 16 + rq * 4;
;             const f32x4 g4 = ld_f4(F.attn_g + l * 1024 + d0);
;             u32x2 o; o.x = pk2(O[qb][db][0] * rstd * g4[0], O[qb][db][1] * rstd * g4[1]); o.y = pk2(O[qb][db][2] * rstd * g4[2], O[qb][db][3] * rstd * g4[3]);
;             st_u2(MIX + (size_t)tq * D + d0, o);
;         }
;     }
	v_pk_mul_f32 v[20:21], v[22:23], v[20:21]
	v_and_b32_sdwa v13, v11, v213 dst_sel:DWORD dst_unused:UNUSED_PAD src0_sel:WORD_1 src1_sel:DWORD
	v_and_b32_sdwa v14, v10, v213 dst_sel:DWORD dst_unused:UNUSED_PAD src0_sel:WORD_1 src1_sel:DWORD
	v_and_b32_sdwa v5, v21, v213 dst_sel:DWORD dst_unused:UNUSED_PAD src0_sel:WORD_1 src1_sel:DWORD
	v_and_b32_sdwa v12, v20, v213 dst_sel:DWORD dst_unused:UNUSED_PAD src0_sel:WORD_1 src1_sel:DWORD
	v_add3_u32 v11, v11, v13, s76
	v_add3_u32 v10, v10, v14, s76
	v_add3_u32 v12, v20, v12, s76
	v_add3_u32 v5, v21, v5, s76
	v_and_b32_e32 v11, 0xffff0000, v11
	v_and_b32_e32 v10, 0xffff0000, v10
	v_or_b32_sdwa v11, v11, v5 dst_sel:DWORD dst_unused:UNUSED_PAD src0_sel:DWORD src1_sel:WORD_1
	v_or_b32_sdwa v10, v10, v12 dst_sel:DWORD dst_unused:UNUSED_PAD src0_sel:DWORD src1_sel:WORD_1
	ds_write_b64 v132, v[10:11] offset:4512
	v_mov_b32_e32 v10, v120
	v_mov_b32_e32 v11, v121
	v_mov_b32_e32 v12, v122
	v_mov_b32_e32 v13, v123
	v_mov_b32_e32 v15, v6
	v_mov_b32_e32 v6, v9
	v_mov_b32_e32 v14, v8
	v_pk_mul_f32 v[6:7], v[6:7], v[4:5] op_sel_hi:[1,0]
	v_pk_mul_f32 v[14:15], v[14:15], v[4:5] op_sel_hi:[1,0]
	v_mov_b32_e32 v17, v12
	v_mov_b32_e32 v12, v11
	v_mov_b32_e32 v16, v10
	v_pk_mul_f32 v[6:7], v[12:13], v[6:7]
	v_pk_mul_f32 v[14:15], v[16:17], v[14:15]
	v_and_b32_sdwa v9, v7, v213 dst_sel:DWORD dst_unused:UNUSED_PAD src0_sel:WORD_1 src1_sel:DWORD
	v_and_b32_sdwa v10, v6, v213 dst_sel:DWORD dst_unused:UNUSED_PAD src0_sel:WORD_1 src1_sel:DWORD
	v_and_b32_sdwa v5, v15, v213 dst_sel:DWORD dst_unused:UNUSED_PAD src0_sel:WORD_1 src1_sel:DWORD
	v_and_b32_sdwa v8, v14, v213 dst_sel:DWORD dst_unused:UNUSED_PAD src0_sel:WORD_1 src1_sel:DWORD
	v_add3_u32 v7, v7, v9, s76
	v_add3_u32 v6, v6, v10, s76
	v_add3_u32 v8, v14, v8, s76
	v_add3_u32 v5, v15, v5, s76
	v_and_b32_e32 v7, 0xffff0000, v7
	v_and_b32_e32 v6, 0xffff0000, v6
	v_or_b32_sdwa v7, v7, v5 dst_sel:DWORD dst_unused:UNUSED_PAD src0_sel:DWORD src1_sel:WORD_1
	v_or_b32_sdwa v6, v6, v8 dst_sel:DWORD dst_unused:UNUSED_PAD src0_sel:DWORD src1_sel:WORD_1
	ds_write_b64 v132, v[6:7] offset:4544
	v_mov_b32_e32 v6, v124
	v_mov_b32_e32 v7, v125
	v_mov_b32_e32 v8, v126
	v_mov_b32_e32 v9, v127
	v_mov_b32_e32 v11, v0
	v_mov_b32_e32 v0, v3
	v_mov_b32_e32 v10, v2
	v_pk_mul_f32 v[0:1], v[0:1], v[4:5] op_sel_hi:[1,0]
	v_pk_mul_f32 v[10:11], v[10:11], v[4:5] op_sel_hi:[1,0]
	v_mov_b32_e32 v13, v8
	v_mov_b32_e32 v8, v7
	v_mov_b32_e32 v12, v6
	v_pk_mul_f32 v[0:1], v[8:9], v[0:1]
	v_pk_mul_f32 v[10:11], v[12:13], v[10:11]
	v_and_b32_sdwa v4, v1, v213 dst_sel:DWORD dst_unused:UNUSED_PAD src0_sel:WORD_1 src1_sel:DWORD
	v_and_b32_sdwa v5, v0, v213 dst_sel:DWORD dst_unused:UNUSED_PAD src0_sel:WORD_1 src1_sel:DWORD
	v_and_b32_sdwa v2, v11, v213 dst_sel:DWORD dst_unused:UNUSED_PAD src0_sel:WORD_1 src1_sel:DWORD
	v_and_b32_sdwa v3, v10, v213 dst_sel:DWORD dst_unused:UNUSED_PAD src0_sel:WORD_1 src1_sel:DWORD
	v_add3_u32 v1, v1, v4, s76
	v_add3_u32 v0, v0, v5, s76
	v_add3_u32 v3, v10, v3, s76
	v_add3_u32 v2, v11, v2, s76
	v_and_b32_e32 v1, 0xffff0000, v1
	v_and_b32_e32 v0, 0xffff0000, v0
	v_or_b32_sdwa v1, v1, v2 dst_sel:DWORD dst_unused:UNUSED_PAD src0_sel:DWORD src1_sel:WORD_1
	v_or_b32_sdwa v0, v0, v3 dst_sel:DWORD dst_unused:UNUSED_PAD src0_sel:DWORD src1_sel:WORD_1
	ds_write_b64 v132, v[0:1] offset:4576
	s_waitcnt lgkmcnt(0)
	ds_read_b128 v[96:99], v133
	ds_read_b128 v[100:103], v133 offset:1088
	ds_read_b128 v[104:107], v133 offset:2176
	ds_read_b128 v[108:111], v133 offset:3264
	ds_read_b128 v[112:115], v133 offset:4352
	ds_read_b128 v[116:119], v133 offset:5440
	ds_read_b128 v[120:123], v133 offset:6528
	ds_read_b128 v[124:127], v133 offset:7616
	v_mov_b32_e32 v136, 0x4000
	v_mov_b32_e32 v137, 0
	s_waitcnt lgkmcnt(7)
	global_store_dwordx4 v[130:131], v[96:99], off
	v_lshl_add_u64 v[130:131], v[130:131], 0, v[136:137]
	s_waitcnt lgkmcnt(6)
	global_store_dwordx4 v[130:131], v[100:103], off
	v_lshl_add_u64 v[130:131], v[130:131], 0, v[136:137]
	s_waitcnt lgkmcnt(5)
	global_store_dwordx4 v[130:131], v[104:107], off
	v_lshl_add_u64 v[130:131], v[130:131], 0, v[136:137]
	s_waitcnt lgkmcnt(4)
	global_store_dwordx4 v[130:131], v[108:111], off
	v_lshl_add_u64 v[130:131], v[130:131], 0, v[136:137]
	s_waitcnt lgkmcnt(3)
	global_store_dwordx4 v[130:131], v[112:115], off
	v_lshl_add_u64 v[130:131], v[130:131], 0, v[136:137]
	s_waitcnt lgkmcnt(2)
	global_store_dwordx4 v[130:131], v[116:119], off
	v_lshl_add_u64 v[130:131], v[130:131], 0, v[136:137]
	s_waitcnt lgkmcnt(1)
	global_store_dwordx4 v[130:131], v[120:123], off
	v_lshl_add_u64 v[130:131], v[130:131], 0, v[136:137]
	s_waitcnt lgkmcnt(0)
	global_store_dwordx4 v[130:131], v[124:127], off
	s_setprio 0
	s_cbranch_scc0 .LBB0_479
